# P8 layer 1: LN2 gamma/beta + gate2 rows from LDS (as layer 0), row data waits counted; stacked
# speedup vs baseline: 1.0352x; 1.0168x over previous
; __device__ __forceinline__ void refresh(Frame& F) { int l = (int)__builtin_amdgcn_mbcnt_hi(~0u, __builtin_amdgcn_mbcnt_lo(~0u, 0u)); asm volatile("" : "+v"(l)); F.lane = l; F.tid = F.wave * 64 + l; }
; template <int l>
; __device__ __forceinline__ void layer_phases(Frame& F, const XcdBarrier& bar, const int lo, const int hi) {
;     ...
;         if (IN(pb + 6)) for (int rep = 0; rep < NREP(8); ++rep) {
;             refresh(F);
;             const unsigned char* yb = ws + WS_YBUF; const bf16* x1 = (const bf16*)(ws + WS_X1); bf16* x2b = (bf16*)(ws + WS_X2B);
;             const int* tinfo = (const int*)(ws + WS_TINFO); const float* gates = (const float*)(ws + WS_GATE);
;             const float* g2 = inptr<const float>(F, I_LN2G) + (size_t)l * D; const float* b2 = inptr<const float>(F, I_LN2B) + (size_t)l * D; float* Fout = inptr<float>(F, I_OUT);
;             auto row_of = [&](const int m_) { return (F.G == 256) ? (2048 * ((m_ >> 3) & 7) + 8 * ((m_ & 2047) >> 6) + (m_ & 7) + 256 * (m_ >> 11)) : m_; };
;             auto load_row = [&](const int m, v4u (&xr)[4], v4u (&yr)[14], float& gtv) {
;                 int ln = F.lane; asm volatile("" : "+v"(ln));
;                 gtv = 0.f; if (ln < 6) gtv = gates[(size_t)m * 6 + ln];
.LBB0_1874:
	s_cmp_gt_i32 s92, 16
	s_cselect_b64 s[0:1], -1, 0
	s_cmp_lt_i32 s93, 17
	s_cselect_b64 s[2:3], -1, 0
	s_or_b64 s[0:1], s[0:1], s[2:3]
	s_and_b64 vcc, exec, s[0:1]
	s_cbranch_vccnz .LBB0_1899
	s_add_i32 s0, 0, 0x21498
	s_waitcnt vmcnt(17)
	v_mov_b32_e32 v0, s0
	s_add_i32 s0, 0, 0x214a8
	v_mov_b32_e32 v200, v216
	s_waitcnt vmcnt(16)
	v_mov_b32_e32 v4, s0
	ds_read2_b64 v[0:3], v0 offset1:1
	ds_read_b64 v[4:5], v4
	s_cmpk_gt_i32 s79, 0x3fff
	s_waitcnt lgkmcnt(1)
	v_readfirstlane_b32 s9, v1
	v_readfirstlane_b32 s8, v0
	v_readfirstlane_b32 s11, v3
	v_readfirstlane_b32 s10, v2
	s_waitcnt lgkmcnt(0)
	v_readfirstlane_b32 s23, v5
	v_readfirstlane_b32 s25, v4
	s_nop 0
	s_lshl_b32 s98, s90, 4
	v_lshl_add_u32 v238, v216, 4, s98
	s_add_u32 s100, s56, 0x16a000
	s_addc_u32 s101, s57, 0
	global_load_dwordx4 v[100:103], v238, s[100:101]
	s_add_u32 s100, s100, 0xc000
	s_addc_u32 s101, s101, 0
	global_load_dwordx4 v[104:107], v238, s[100:101]
	s_add_u32 s100, s100, 0xc000
	s_addc_u32 s101, s101, 0
	global_load_dwordx4 v[108:111], v238, s[100:101]
	s_add_u32 s100, s100, 0xc000
	s_addc_u32 s101, s101, 0
	global_load_dwordx4 v[112:115], v238, s[100:101]
	s_add_u32 s100, s100, 0xc000
	s_addc_u32 s101, s101, 0
	global_load_dwordx4 v[116:119], v238, s[100:101]
	s_add_u32 s100, s100, 0xc000
	s_addc_u32 s101, s101, 0
	global_load_dwordx4 v[120:123], v238, s[100:101]
	s_add_u32 s100, s100, 0xc000
	s_addc_u32 s101, s101, 0
	global_load_dwordx4 v[124:127], v238, s[100:101]
	s_add_u32 s100, s100, 0xc000
	s_addc_u32 s101, s101, 0
	global_load_dwordx4 v[128:131], v238, s[100:101]
	s_add_u32 s100, s8, 0x2000
	s_addc_u32 s101, s9, 0
	global_load_dwordx4 v[132:135], v238, s[100:101]
	s_add_u32 s100, s10, 0x2000
	s_addc_u32 s101, s11, 0
	global_load_dwordx4 v[136:139], v238, s[100:101]
	v_add_u32_e32 v239, 0x10000, v238
	s_waitcnt vmcnt(9)
	ds_write_b128 v238, v[100:103] offset:0
	s_waitcnt vmcnt(8)
	ds_write_b128 v238, v[104:107] offset:8192
	s_waitcnt vmcnt(7)
	ds_write_b128 v238, v[108:111] offset:16384
	s_waitcnt vmcnt(6)
	ds_write_b128 v238, v[112:115] offset:24576
	s_waitcnt vmcnt(5)
	ds_write_b128 v238, v[116:119] offset:32768
	s_waitcnt vmcnt(4)
	ds_write_b128 v238, v[120:123] offset:40960
	s_waitcnt vmcnt(3)
	ds_write_b128 v238, v[124:127] offset:49152
	s_waitcnt vmcnt(2)
	ds_write_b128 v238, v[128:131] offset:57344
	s_waitcnt vmcnt(1)
	ds_write_b128 v239, v[132:135]
	s_waitcnt vmcnt(0)
	ds_write_b128 v239, v[136:139] offset:8192
	s_sub_u32 s98, 0xe000, s8
	s_sub_u32 s99, 0x10000, s10
	s_waitcnt lgkmcnt(0)
	s_barrier
	s_cmpk_gt_i32 s79, 0x3fff
	s_cbranch_scc1 .LBB0_1898
	s_add_u32 s39, s56, 0x900000
	s_addc_u32 s41, s57, 0
	s_ashr_i32 s0, s79, 3
	s_lshr_b32 s1, s79, 3
	s_and_b32 s0, s0, 0xffffff00
	s_and_b32 s1, s1, 0xf8
	s_lshl_b32 s45, s79, 8
	s_bfe_u32 s43, s90, 0x30006
	s_or_b32 s0, s0, s1
	s_and_b32 s1, s45, 0x3800
	s_or_b32 s1, s1, s43
	s_add_i32 s2, s1, s0
	s_cmpk_eq_i32 s76, 0x100
	s_cselect_b64 s[4:5], -1, 0
	s_and_b64 s[0:1], s[4:5], exec
	s_cselect_b32 s0, s2, s79
	v_mov_b32_e32 v0, v200
	s_ashr_i32 s1, s0, 31
	v_cmp_gt_i32_e32 vcc, 6, v0
	v_mov_b32_e32 v201, 0
	v_mov_b32_e32 v202, 0
	s_and_saveexec_b64 s[2:3], vcc
	s_cbranch_execz .LBB0_1878
	s_mul_i32 s6, s0, 24
	s_mul_hi_i32 s7, s0, 24
	s_add_u32 s6, s39, s6
	v_ashrrev_i32_e32 v1, 31, v0
	s_addc_u32 s7, s41, s7
	v_lshl_add_u64 v[2:3], v[0:1], 2, s[6:7]
	global_load_dword v202, v[2:3], off

; #define GAS __attribute__((address_space(1)))
; __device__ __forceinline__ f32x4 bf4(unsigned a, unsigned b) { return (f32x4){bflo(a), bfhi(a), bflo(b), bfhi(b)}; }
; template <int l>
; __device__ __forceinline__ void layer_phases(Frame& F, const XcdBarrier& bar, const int lo, const int hi) {
;     ...
;             auto process_row = [&](const int m, v4u (&xr)[4], v4u (&yr)[14], const float gtv) {
;                 int ln = F.lane; asm volatile("" : "+v"(ln));
;                 const float* mrow = (const float*)(ws + WS_MOD) + ((size_t)l * 8 + (m >> 11)) * 12288;
;                 float gt[7];
; #pragma unroll
;                 for (int k = 0; k < 6; ++k) gt[k] = __uint_as_float((unsigned)__builtin_amdgcn_readlane((int)__float_as_uint(gtv), k));
;                 gt[6] = 1.0f;
;                 f32x4 v[8]; float s = 0.f;
; #pragma unroll
;                 for (int jh = 0; jh < 2; ++jh) { const v4u xa = xr[2 * jh], xb = xr[2 * jh + 1];
;                     v[4 * jh] = bf4(xa.x, xa.y); v[4 * jh + 1] = bf4(xa.z, xa.w); v[4 * jh + 2] = bf4(xb.x, xb.y); v[4 * jh + 3] = bf4(xb.z, xb.w); }
; #pragma unroll
;                 for (int jh = 0; jh < 2; ++jh) {
; #pragma unroll
;                     for (int i = 0; i < 4; ++i) { const int j = 4 * jh + i, k = 16 * ln + 1024 * jh + 4 * i; f32x4 f = (f32x4){0.f, 0.f, 0.f, 0.f};
; #pragma unroll
;                         for (int q = 0; q < 7; ++q) { const unsigned w = yr[7 * jh + q][i]; const float gq = gt[q];
;                             const auto lo2 = __builtin_amdgcn_cvt_pk_f32_fp8((int)w, false), hi2 = __builtin_amdgcn_cvt_pk_f32_fp8((int)w, true);
;                             f.x += gq * lo2[0]; f.y += gq * lo2[1]; f.z += gq * hi2[0]; f.w += gq * hi2[1]; }
;                         v[j] = v[j] * ALPHA + *(const GAS f32x4*)(mrow + 10240 + k) * (f * (1.0f / (float)(1 << YSHIFT)));
;                         s += (v[j].x + v[j].y) + (v[j].z + v[j].w); }
.LBB0_1879:
	s_ashr_i32 s0, s28, 11
	s_lshl_b32 s100, s0, 13
	v_mov_b32_e32 v144, v200
	s_add_i32 s0, s0, 8
	s_mul_hi_i32 s1, s0, 0xc000
	s_mul_i32 s0, s0, 0xc000
	v_lshlrev_b32_e32 v160, 4, v144
	s_add_u32 s0, s56, s0
	v_ashrrev_i32_e32 v161, 31, v160
	s_addc_u32 s1, s57, s1
	s_sub_u32 s100, s100, s0
	s_sub_u32 s100, s100, 0x10a000
	v_lshlrev_b64 v[162:163], 2, v[160:161]
	v_lshl_add_u64 v[180:181], s[0:1], 0, v[162:163]
	v_add_co_u32_e32 v194, vcc, s54, v180
	v_lshl_add_u64 v[144:145], v[180:181], 0, s[20:21]
	s_nop 0
	v_addc_co_u32_e32 v195, vcc, 0, v181, vcc
	v_add_u32_e32 v247, s100, v194
	v_add_u32_e32 v247, 0xfffff000, v247
	ds_read_b128 v[156:159], v247
	v_add_u32_e32 v247, s100, v144
	ds_read_b128 v[148:151], v247 offset:32
	v_add_u32_e32 v247, s100, v144
	ds_read_b128 v[152:155], v247 offset:16
	v_cvt_pk_f32_fp8_e32 v[146:147], v100
	v_cvt_pk_f32_fp8_e32 v[214:215], v104
	v_cvt_pk_f32_fp8_e32 v[218:219], v96
	v_readlane_b32 s40, v201, 0
	v_cvt_pk_f32_fp8_e32 v[222:223], v112
	v_readlane_b32 s38, v201, 1
	v_cvt_pk_f32_fp8_e32 v[226:227], v88
	v_pk_fma_f32 v[146:147], s[40:41], v[146:147], 0 op_sel_hi:[0,1,0]
	v_readlane_b32 s36, v201, 2
	v_cvt_pk_f32_fp8_e32 v[230:231], v92
	v_pk_fma_f32 v[146:147], s[38:39], v[214:215], v[146:147] op_sel_hi:[0,1,1]
	v_readlane_b32 s34, v201, 3
	v_cvt_pk_f32_fp8_e32 v[234:235], v108
	v_pk_fma_f32 v[146:147], s[36:37], v[218:219], v[146:147] op_sel_hi:[0,1,1]
	v_readlane_b32 s30, v201, 4
	v_pk_fma_f32 v[146:147], s[34:35], v[222:223], v[146:147] op_sel_hi:[0,1,1]
	v_readlane_b32 s0, v201, 5
	v_pk_fma_f32 v[146:147], s[30:31], v[226:227], v[146:147] op_sel_hi:[0,1,1]
	v_cvt_pk_f32_fp8_sdwa v[212:213], v100 src0_sel:WORD_1
	v_pk_fma_f32 v[146:147], s[0:1], v[230:231], v[146:147] op_sel_hi:[0,1,1]
	v_pk_add_f32 v[214:215], v[146:147], v[234:235]
	v_add_u32_e32 v247, s100, v144
	ds_read_b128 v[144:147], v247 offset:48
	v_cvt_pk_f32_fp8_sdwa v[216:217], v104 src0_sel:WORD_1
	v_cvt_pk_f32_fp8_sdwa v[220:221], v96 src0_sel:WORD_1
	v_cvt_pk_f32_fp8_sdwa v[224:225], v112 src0_sel:WORD_1
	v_cvt_pk_f32_fp8_sdwa v[228:229], v88 src0_sel:WORD_1
	v_pk_fma_f32 v[212:213], s[40:41], v[212:213], 0 op_sel_hi:[0,1,0]
	v_cvt_pk_f32_fp8_sdwa v[232:233], v92 src0_sel:WORD_1
	v_pk_fma_f32 v[212:213], s[38:39], v[216:217], v[212:213] op_sel_hi:[0,1,1]
	v_cvt_pk_f32_fp8_sdwa v[236:237], v108 src0_sel:WORD_1
	v_pk_fma_f32 v[212:213], s[36:37], v[220:221], v[212:213] op_sel_hi:[0,1,1]
	v_pk_fma_f32 v[212:213], s[34:35], v[224:225], v[212:213] op_sel_hi:[0,1,1]
	v_pk_fma_f32 v[212:213], s[30:31], v[228:229], v[212:213] op_sel_hi:[0,1,1]
	v_pk_fma_f32 v[212:213], s[0:1], v[232:233], v[212:213] op_sel_hi:[0,1,1]
	v_pk_add_f32 v[212:213], v[212:213], v[236:237]
	v_pk_mul_f32 v[216:217], v[214:215], s[22:23] op_sel_hi:[1,0]
	v_pk_mul_f32 v[218:219], v[212:213], s[22:23] op_sel_hi:[1,0]
	v_lshlrev_b32_e32 v196, 16, v68
	v_and_b32_e32 v197, 0xffff0000, v68
	v_lshlrev_b32_e32 v198, 16, v69
	v_and_b32_e32 v199, 0xffff0000, v69
	v_add_u32_e32 v247, s100, v194
	ds_read_b128 v[212:215], v247
	v_cvt_pk_f32_fp8_sdwa v[220:221], v97 src0_sel:WORD_1
	v_cvt_pk_f32_fp8_e32 v[222:223], v113
	v_cvt_pk_f32_fp8_sdwa v[224:225], v113 src0_sel:WORD_1
	v_cvt_pk_f32_fp8_e32 v[226:227], v89
	v_cvt_pk_f32_fp8_sdwa v[228:229], v89 src0_sel:WORD_1
	v_cvt_pk_f32_fp8_e32 v[230:231], v93
	v_cvt_pk_f32_fp8_sdwa v[232:233], v93 src0_sel:WORD_1
	v_cvt_pk_f32_fp8_e32 v[234:235], v109
	v_cvt_pk_f32_fp8_sdwa v[236:237], v109 src0_sel:WORD_1
	v_lshlrev_b32_e32 v190, 16, v70
	v_and_b32_e32 v191, 0xffff0000, v70
	v_lshlrev_b32_e32 v192, 16, v71
	v_and_b32_e32 v193, 0xffff0000, v71
	v_lshlrev_b32_e32 v186, 16, v72
	v_and_b32_e32 v187, 0xffff0000, v72
	v_lshlrev_b32_e32 v188, 16, v73
	v_and_b32_e32 v189, 0xffff0000, v73
	v_lshlrev_b32_e32 v182, 16, v74
	v_and_b32_e32 v183, 0xffff0000, v74
	v_lshlrev_b32_e32 v184, 16, v75
	v_and_b32_e32 v185, 0xffff0000, v75
	v_lshlrev_b32_e32 v170, 16, v80
	v_and_b32_e32 v171, 0xffff0000, v80
	v_lshlrev_b32_e32 v168, 16, v81
	v_and_b32_e32 v169, 0xffff0000, v81
	v_lshlrev_b32_e32 v176, 16, v82
	v_and_b32_e32 v177, 0xffff0000, v82
	v_lshlrev_b32_e32 v174, 16, v83
	v_and_b32_e32 v175, 0xffff0000, v83
	v_lshlrev_b32_e32 v178, 16, v85
	v_and_b32_e32 v179, 0xffff0000, v85
	v_lshlrev_b32_e32 v172, 16, v84
	v_and_b32_e32 v173, 0xffff0000, v84
	v_lshlrev_b32_e32 v164, 16, v86
	v_and_b32_e32 v165, 0xffff0000, v86
	v_lshlrev_b32_e32 v166, 16, v87
	s_waitcnt lgkmcnt(0)
	v_pk_mul_f32 v[158:159], v[158:159], v[218:219]
	v_pk_mul_f32 v[194:195], v[156:157], v[216:217]
	v_pk_fma_f32 v[156:157], v[198:199], s[24:25], v[158:159] op_sel_hi:[1,0,1]
	v_pk_fma_f32 v[158:159], v[196:197], s[24:25], v[194:195] op_sel_hi:[1,0,1]
	v_cvt_pk_f32_fp8_e32 v[194:195], v101
	v_cvt_pk_f32_fp8_sdwa v[196:197], v101 src0_sel:WORD_1
	v_cvt_pk_f32_fp8_e32 v[198:199], v105
	v_cvt_pk_f32_fp8_sdwa v[216:217], v105 src0_sel:WORD_1
	v_cvt_pk_f32_fp8_e32 v[218:219], v97
	v_pk_fma_f32 v[196:197], s[40:41], v[196:197], 0 op_sel_hi:[0,1,0]
	v_pk_fma_f32 v[194:195], s[40:41], v[194:195], 0 op_sel_hi:[0,1,0]
	v_pk_fma_f32 v[194:195], s[38:39], v[198:199], v[194:195] op_sel_hi:[0,1,1]
	v_pk_fma_f32 v[196:197], s[38:39], v[216:217], v[196:197] op_sel_hi:[0,1,1]
	v_pk_fma_f32 v[196:197], s[36:37], v[220:221], v[196:197] op_sel_hi:[0,1,1]
	v_pk_fma_f32 v[194:195], s[36:37], v[218:219], v[194:195] op_sel_hi:[0,1,1]
	v_pk_fma_f32 v[194:195], s[34:35], v[222:223], v[194:195] op_sel_hi:[0,1,1]
	v_pk_fma_f32 v[196:197], s[34:35], v[224:225], v[196:197] op_sel_hi:[0,1,1]
	v_pk_fma_f32 v[196:197], s[30:31], v[228:229], v[196:197] op_sel_hi:[0,1,1]
	v_pk_fma_f32 v[194:195], s[30:31], v[226:227], v[194:195] op_sel_hi:[0,1,1]
	v_pk_fma_f32 v[194:195], s[0:1], v[230:231], v[194:195] op_sel_hi:[0,1,1]
	v_pk_fma_f32 v[196:197], s[0:1], v[232:233], v[196:197] op_sel_hi:[0,1,1]
	v_pk_add_f32 v[196:197], v[196:197], v[236:237]
	v_pk_add_f32 v[194:195], v[194:195], v[234:235]
	v_pk_mul_f32 v[196:197], v[196:197], s[22:23] op_sel_hi:[1,0]
	v_pk_mul_f32 v[194:195], v[194:195], s[22:23] op_sel_hi:[1,0]
	s_waitcnt lgkmcnt(0)
; #define GAS __attribute__((address_space(1)))
; template <int l>
; __device__ __forceinline__ void layer_phases(Frame& F, const XcdBarrier& bar, const int lo, const int hi) {
;     ...
;                 for (int jh = 0; jh < 2; ++jh) {
; #pragma unroll
;                     for (int i = 0; i < 4; ++i) { const int j = 4 * jh + i, k = 16 * ln + 1024 * jh + 4 * i; f32x4 f = (f32x4){0.f, 0.f, 0.f, 0.f};
; #pragma unroll
;                         for (int q = 0; q < 7; ++q) { const unsigned w = yr[7 * jh + q][i]; const float gq = gt[q];
;                             const auto lo2 = __builtin_amdgcn_cvt_pk_f32_fp8((int)w, false), hi2 = __builtin_amdgcn_cvt_pk_f32_fp8((int)w, true);
;                             f.x += gq * lo2[0]; f.y += gq * lo2[1]; f.z += gq * hi2[0]; f.w += gq * hi2[1]; }
;                         v[j] = v[j] * ALPHA + *(const GAS f32x4*)(mrow + 10240 + k) * (f * (1.0f / (float)(1 << YSHIFT)));
;                         s += (v[j].x + v[j].y) + (v[j].z + v[j].w); }
	v_pk_mul_f32 v[154:155], v[154:155], v[196:197]
	v_pk_mul_f32 v[194:195], v[152:153], v[194:195]
	v_pk_fma_f32 v[152:153], v[192:193], s[24:25], v[154:155] op_sel_hi:[1,0,1]
	v_pk_fma_f32 v[154:155], v[190:191], s[24:25], v[194:195] op_sel_hi:[1,0,1]
	v_mov_b32_e32 v190, v158
	v_mov_b32_e32 v191, v154
	v_mov_b32_e32 v192, v159
	v_mov_b32_e32 v193, v155
	v_pk_add_f32 v[190:191], v[190:191], v[192:193]
	v_mov_b32_e32 v192, v156
	v_mov_b32_e32 v193, v152
	v_mov_b32_e32 v194, v157
	v_mov_b32_e32 v195, v153
	v_pk_add_f32 v[192:193], v[192:193], v[194:195]
	v_cvt_pk_f32_fp8_e32 v[196:197], v106
	v_pk_add_f32 v[190:191], v[190:191], v[192:193]
	v_cvt_pk_f32_fp8_sdwa v[192:193], v102 src0_sel:WORD_1
	v_add_f32_e32 v161, 0, v190
	v_add_f32_e32 v194, v161, v191
	v_cvt_pk_f32_fp8_e32 v[190:191], v102
	v_cvt_pk_f32_fp8_sdwa v[198:199], v106 src0_sel:WORD_1
	v_cvt_pk_f32_fp8_e32 v[216:217], v98
	v_cvt_pk_f32_fp8_sdwa v[218:219], v98 src0_sel:WORD_1
	v_cvt_pk_f32_fp8_e32 v[220:221], v114
	v_cvt_pk_f32_fp8_sdwa v[222:223], v114 src0_sel:WORD_1
	v_cvt_pk_f32_fp8_e32 v[224:225], v90
	v_cvt_pk_f32_fp8_sdwa v[226:227], v90 src0_sel:WORD_1
	v_pk_fma_f32 v[192:193], s[40:41], v[192:193], 0 op_sel_hi:[0,1,0]
	v_pk_fma_f32 v[190:191], s[40:41], v[190:191], 0 op_sel_hi:[0,1,0]
	v_cvt_pk_f32_fp8_e32 v[228:229], v94
	v_cvt_pk_f32_fp8_sdwa v[230:231], v94 src0_sel:WORD_1
	v_pk_fma_f32 v[190:191], s[38:39], v[196:197], v[190:191] op_sel_hi:[0,1,1]
	v_pk_fma_f32 v[192:193], s[38:39], v[198:199], v[192:193] op_sel_hi:[0,1,1]
	v_cvt_pk_f32_fp8_e32 v[232:233], v110
	v_cvt_pk_f32_fp8_sdwa v[234:235], v110 src0_sel:WORD_1
	v_pk_fma_f32 v[192:193], s[36:37], v[218:219], v[192:193] op_sel_hi:[0,1,1]
	v_pk_fma_f32 v[190:191], s[36:37], v[216:217], v[190:191] op_sel_hi:[0,1,1]
	v_pk_fma_f32 v[190:191], s[34:35], v[220:221], v[190:191] op_sel_hi:[0,1,1]
	v_pk_fma_f32 v[192:193], s[34:35], v[222:223], v[192:193] op_sel_hi:[0,1,1]
	v_pk_fma_f32 v[192:193], s[30:31], v[226:227], v[192:193] op_sel_hi:[0,1,1]
	v_pk_fma_f32 v[190:191], s[30:31], v[224:225], v[190:191] op_sel_hi:[0,1,1]
	v_pk_fma_f32 v[190:191], s[0:1], v[228:229], v[190:191] op_sel_hi:[0,1,1]
	v_pk_fma_f32 v[192:193], s[0:1], v[230:231], v[192:193] op_sel_hi:[0,1,1]
	v_pk_add_f32 v[192:193], v[192:193], v[234:235]
	v_pk_add_f32 v[190:191], v[190:191], v[232:233]
	v_pk_mul_f32 v[192:193], v[192:193], s[22:23] op_sel_hi:[1,0]
	v_pk_mul_f32 v[190:191], v[190:191], s[22:23] op_sel_hi:[1,0]
	v_pk_mul_f32 v[150:151], v[150:151], v[192:193]
	v_pk_mul_f32 v[148:149], v[148:149], v[190:191]
	v_pk_fma_f32 v[150:151], v[188:189], s[24:25], v[150:151] op_sel_hi:[1,0,1]
	v_pk_fma_f32 v[148:149], v[186:187], s[24:25], v[148:149] op_sel_hi:[1,0,1]
	v_mov_b32_e32 v189, v151
	v_pk_mov_b32 v[186:187], v[148:149], v[150:151] op_sel:[1,0]
	v_mov_b32_e32 v188, v148
	v_pk_add_f32 v[186:187], v[186:187], v[188:189]
	v_cvt_pk_f32_fp8_sdwa v[188:189], v103 src0_sel:WORD_1
	v_pk_add_f32 v[196:197], v[186:187], v[186:187] op_sel:[0,1] op_sel_hi:[1,0]
	v_cvt_pk_f32_fp8_e32 v[186:187], v103
	v_cvt_pk_f32_fp8_e32 v[190:191], v107
	v_cvt_pk_f32_fp8_sdwa v[192:193], v107 src0_sel:WORD_1
	v_cvt_pk_f32_fp8_e32 v[198:199], v99
	v_cvt_pk_f32_fp8_sdwa v[216:217], v99 src0_sel:WORD_1
	v_cvt_pk_f32_fp8_e32 v[218:219], v115
	v_cvt_pk_f32_fp8_sdwa v[220:221], v115 src0_sel:WORD_1
	v_cvt_pk_f32_fp8_e32 v[222:223], v91
	v_cvt_pk_f32_fp8_sdwa v[224:225], v91 src0_sel:WORD_1
	v_pk_fma_f32 v[188:189], s[40:41], v[188:189], 0 op_sel_hi:[0,1,0]
	v_pk_fma_f32 v[186:187], s[40:41], v[186:187], 0 op_sel_hi:[0,1,0]
	v_cvt_pk_f32_fp8_e32 v[226:227], v95
	v_cvt_pk_f32_fp8_sdwa v[228:229], v95 src0_sel:WORD_1
	v_pk_fma_f32 v[186:187], s[38:39], v[190:191], v[186:187] op_sel_hi:[0,1,1]
	v_pk_fma_f32 v[188:189], s[38:39], v[192:193], v[188:189] op_sel_hi:[0,1,1]
	v_cvt_pk_f32_fp8_e32 v[230:231], v111
	v_cvt_pk_f32_fp8_sdwa v[232:233], v111 src0_sel:WORD_1
	v_pk_fma_f32 v[188:189], s[36:37], v[216:217], v[188:189] op_sel_hi:[0,1,1]
	v_pk_fma_f32 v[186:187], s[36:37], v[198:199], v[186:187] op_sel_hi:[0,1,1]
	v_pk_fma_f32 v[186:187], s[34:35], v[218:219], v[186:187] op_sel_hi:[0,1,1]
	v_pk_fma_f32 v[188:189], s[34:35], v[220:221], v[188:189] op_sel_hi:[0,1,1]
	v_pk_fma_f32 v[188:189], s[30:31], v[224:225], v[188:189] op_sel_hi:[0,1,1]
	v_pk_fma_f32 v[186:187], s[30:31], v[222:223], v[186:187] op_sel_hi:[0,1,1]
	v_pk_fma_f32 v[186:187], s[0:1], v[226:227], v[186:187] op_sel_hi:[0,1,1]
	v_pk_fma_f32 v[188:189], s[0:1], v[228:229], v[188:189] op_sel_hi:[0,1,1]
	v_pk_add_f32 v[188:189], v[188:189], v[232:233]
	v_pk_add_f32 v[186:187], v[186:187], v[230:231]
	v_lshl_add_u64 v[198:199], v[180:181], 0, s[26:27]
	v_pk_mul_f32 v[190:191], v[186:187], s[22:23] op_sel_hi:[1,0]
	v_pk_mul_f32 v[192:193], v[188:189], s[22:23] op_sel_hi:[1,0]
	v_add_u32_e32 v247, s100, v198
	ds_read_b128 v[186:189], v247 offset:16
	s_waitcnt lgkmcnt(0)
; #define GAS __attribute__((address_space(1)))
; template <int l>
; __device__ __forceinline__ void layer_phases(Frame& F, const XcdBarrier& bar, const int lo, const int hi) {
;     ...
;                 for (int jh = 0; jh < 2; ++jh) {
; #pragma unroll
;                     for (int i = 0; i < 4; ++i) { const int j = 4 * jh + i, k = 16 * ln + 1024 * jh + 4 * i; f32x4 f = (f32x4){0.f, 0.f, 0.f, 0.f};
; #pragma unroll
;                         for (int q = 0; q < 7; ++q) { const unsigned w = yr[7 * jh + q][i]; const float gq = gt[q];
;                             const auto lo2 = __builtin_amdgcn_cvt_pk_f32_fp8((int)w, false), hi2 = __builtin_amdgcn_cvt_pk_f32_fp8((int)w, true);
;                             f.x += gq * lo2[0]; f.y += gq * lo2[1]; f.z += gq * hi2[0]; f.w += gq * hi2[1]; }
;                         v[j] = v[j] * ALPHA + *(const GAS f32x4*)(mrow + 10240 + k) * (f * (1.0f / (float)(1 << YSHIFT)));
;                         s += (v[j].x + v[j].y) + (v[j].z + v[j].w); }
	v_pk_mul_f32 v[144:145], v[144:145], v[190:191]
	v_cvt_pk_f32_fp8_e32 v[180:181], v116
	v_pk_fma_f32 v[144:145], v[182:183], s[24:25], v[144:145] op_sel_hi:[1,0,1]
	v_cvt_pk_f32_fp8_sdwa v[182:183], v116 src0_sel:WORD_1
	v_pk_mul_f32 v[146:147], v[146:147], v[192:193]
	v_cvt_pk_f32_fp8_e32 v[190:191], v120
	v_cvt_pk_f32_fp8_sdwa v[192:193], v120 src0_sel:WORD_1
	v_cvt_pk_f32_fp8_e32 v[218:219], v124
	v_cvt_pk_f32_fp8_sdwa v[220:221], v124 src0_sel:WORD_1
	v_cvt_pk_f32_fp8_e32 v[222:223], v128
	v_cvt_pk_f32_fp8_sdwa v[224:225], v128 src0_sel:WORD_1
	v_cvt_pk_f32_fp8_e32 v[226:227], v132
	v_cvt_pk_f32_fp8_sdwa v[228:229], v132 src0_sel:WORD_1
	v_pk_fma_f32 v[182:183], s[40:41], v[182:183], 0 op_sel_hi:[0,1,0]
	v_pk_fma_f32 v[180:181], s[40:41], v[180:181], 0 op_sel_hi:[0,1,0]
	v_cvt_pk_f32_fp8_e32 v[230:231], v136
	v_cvt_pk_f32_fp8_sdwa v[232:233], v136 src0_sel:WORD_1
	v_pk_fma_f32 v[180:181], s[38:39], v[190:191], v[180:181] op_sel_hi:[0,1,1]
	v_pk_fma_f32 v[182:183], s[38:39], v[192:193], v[182:183] op_sel_hi:[0,1,1]
	v_cvt_pk_f32_fp8_e32 v[234:235], v140
	v_cvt_pk_f32_fp8_sdwa v[236:237], v140 src0_sel:WORD_1
	v_pk_fma_f32 v[182:183], s[36:37], v[220:221], v[182:183] op_sel_hi:[0,1,1]
	v_pk_fma_f32 v[180:181], s[36:37], v[218:219], v[180:181] op_sel_hi:[0,1,1]
	v_pk_fma_f32 v[180:181], s[34:35], v[222:223], v[180:181] op_sel_hi:[0,1,1]
	v_pk_fma_f32 v[182:183], s[34:35], v[224:225], v[182:183] op_sel_hi:[0,1,1]
	v_pk_fma_f32 v[182:183], s[30:31], v[228:229], v[182:183] op_sel_hi:[0,1,1]
	v_pk_fma_f32 v[180:181], s[30:31], v[226:227], v[180:181] op_sel_hi:[0,1,1]
	v_pk_fma_f32 v[180:181], s[0:1], v[230:231], v[180:181] op_sel_hi:[0,1,1]
	v_pk_fma_f32 v[182:183], s[0:1], v[232:233], v[182:183] op_sel_hi:[0,1,1]
	v_pk_add_f32 v[218:219], v[182:183], v[236:237]
	v_pk_add_f32 v[220:221], v[180:181], v[234:235]
	v_add_u32_e32 v247, s100, v198
	ds_read_b128 v[180:183], v247 offset:48
	v_add_u32_e32 v247, s100, v198
	ds_read_b128 v[190:193], v247 offset:32
	v_pk_mul_f32 v[198:199], v[220:221], s[22:23] op_sel_hi:[1,0]
	v_pk_mul_f32 v[218:219], v[218:219], s[22:23] op_sel_hi:[1,0]
	s_waitcnt lgkmcnt(0)
	v_pk_mul_f32 v[198:199], v[212:213], v[198:199]
	v_pk_mul_f32 v[214:215], v[214:215], v[218:219]
	v_pk_fma_f32 v[146:147], v[184:185], s[24:25], v[146:147] op_sel_hi:[1,0,1]
	v_pk_fma_f32 v[168:169], v[168:169], s[24:25], v[214:215] op_sel_hi:[1,0,1]
	v_pk_fma_f32 v[170:171], v[170:171], s[24:25], v[198:199] op_sel_hi:[1,0,1]
	v_add_f32_e32 v184, v144, v145
	v_add_f32_e32 v216, v146, v147
	v_mov_b32_e32 v195, v170
	v_mov_b32_e32 v197, v171
	v_mov_b32_e32 v185, v168
	v_mov_b32_e32 v217, v169
	v_pk_add_f32 v[194:195], v[194:195], v[196:197]
	v_pk_add_f32 v[184:185], v[184:185], v[216:217]
	v_cvt_pk_f32_fp8_e32 v[198:199], v121
	v_pk_add_f32 v[184:185], v[194:195], v[184:185]
	v_cvt_pk_f32_fp8_e32 v[194:195], v117
	v_cvt_pk_f32_fp8_e32 v[214:215], v125
	v_cvt_pk_f32_fp8_e32 v[218:219], v129
	v_cvt_pk_f32_fp8_e32 v[222:223], v133
	v_pk_fma_f32 v[194:195], s[40:41], v[194:195], 0 op_sel_hi:[0,1,0]
	v_cvt_pk_f32_fp8_e32 v[226:227], v137
	v_pk_fma_f32 v[194:195], s[38:39], v[198:199], v[194:195] op_sel_hi:[0,1,1]
	v_cvt_pk_f32_fp8_sdwa v[196:197], v117 src0_sel:WORD_1
	v_cvt_pk_f32_fp8_e32 v[230:231], v141
	v_pk_fma_f32 v[194:195], s[36:37], v[214:215], v[194:195] op_sel_hi:[0,1,1]
	v_cvt_pk_f32_fp8_sdwa v[212:213], v121 src0_sel:WORD_1
	v_pk_fma_f32 v[194:195], s[34:35], v[218:219], v[194:195] op_sel_hi:[0,1,1]
	v_cvt_pk_f32_fp8_sdwa v[216:217], v125 src0_sel:WORD_1
	v_pk_fma_f32 v[194:195], s[30:31], v[222:223], v[194:195] op_sel_hi:[0,1,1]
	v_cvt_pk_f32_fp8_sdwa v[220:221], v129 src0_sel:WORD_1
	v_pk_fma_f32 v[194:195], s[0:1], v[226:227], v[194:195] op_sel_hi:[0,1,1]
	v_cvt_pk_f32_fp8_sdwa v[224:225], v133 src0_sel:WORD_1
	v_pk_fma_f32 v[196:197], s[40:41], v[196:197], 0 op_sel_hi:[0,1,0]
	v_pk_add_f32 v[194:195], v[194:195], v[230:231]
	v_cvt_pk_f32_fp8_sdwa v[228:229], v137 src0_sel:WORD_1
	v_pk_fma_f32 v[196:197], s[38:39], v[212:213], v[196:197] op_sel_hi:[0,1,1]
	v_pk_mul_f32 v[194:195], v[194:195], s[22:23] op_sel_hi:[1,0]
	v_cvt_pk_f32_fp8_sdwa v[232:233], v141 src0_sel:WORD_1
	v_pk_fma_f32 v[196:197], s[36:37], v[216:217], v[196:197] op_sel_hi:[0,1,1]
	v_pk_fma_f32 v[196:197], s[34:35], v[220:221], v[196:197] op_sel_hi:[0,1,1]
	v_cvt_pk_f32_fp8_sdwa v[198:199], v122 src0_sel:WORD_1
	v_pk_fma_f32 v[196:197], s[30:31], v[224:225], v[196:197] op_sel_hi:[0,1,1]
	v_cvt_pk_f32_fp8_sdwa v[214:215], v126 src0_sel:WORD_1
	v_pk_fma_f32 v[196:197], s[0:1], v[228:229], v[196:197] op_sel_hi:[0,1,1]
	v_cvt_pk_f32_fp8_sdwa v[218:219], v130 src0_sel:WORD_1
	s_waitcnt lgkmcnt(0)
	v_pk_mul_f32 v[186:187], v[186:187], v[194:195]
	v_cvt_pk_f32_fp8_sdwa v[194:195], v118 src0_sel:WORD_1
	v_pk_add_f32 v[196:197], v[196:197], v[232:233]
	v_cvt_pk_f32_fp8_sdwa v[222:223], v134 src0_sel:WORD_1
	v_pk_mul_f32 v[196:197], v[196:197], s[22:23] op_sel_hi:[1,0]
	v_pk_fma_f32 v[194:195], s[40:41], v[194:195], 0 op_sel_hi:[0,1,0]
	v_cvt_pk_f32_fp8_sdwa v[226:227], v138 src0_sel:WORD_1
	v_pk_fma_f32 v[194:195], s[38:39], v[198:199], v[194:195] op_sel_hi:[0,1,1]
	v_pk_mul_f32 v[188:189], v[188:189], v[196:197]
	v_cvt_pk_f32_fp8_sdwa v[230:231], v142 src0_sel:WORD_1
	v_pk_fma_f32 v[194:195], s[36:37], v[214:215], v[194:195] op_sel_hi:[0,1,1]
	v_pk_fma_f32 v[174:175], v[174:175], s[24:25], v[188:189] op_sel_hi:[1,0,1]
	v_pk_fma_f32 v[176:177], v[176:177], s[24:25], v[186:187] op_sel_hi:[1,0,1]
	v_pk_fma_f32 v[194:195], s[34:35], v[218:219], v[194:195] op_sel_hi:[0,1,1]
	v_pk_mov_b32 v[186:187], v[176:177], v[174:175] op_sel:[1,0]
	v_mov_b32_e32 v188, v176
	v_mov_b32_e32 v189, v175
	v_pk_fma_f32 v[194:195], s[30:31], v[222:223], v[194:195] op_sel_hi:[0,1,1]
	v_pk_add_f32 v[186:187], v[186:187], v[188:189]
	v_cvt_pk_f32_fp8_e32 v[188:189], v118
	v_pk_fma_f32 v[194:195], s[0:1], v[226:227], v[194:195] op_sel_hi:[0,1,1]
	v_cvt_pk_f32_fp8_e32 v[196:197], v122
	v_pk_add_f32 v[194:195], v[194:195], v[230:231]
	v_cvt_pk_f32_fp8_e32 v[212:213], v126
	v_pk_mul_f32 v[194:195], v[194:195], s[22:23] op_sel_hi:[1,0]
	v_cvt_pk_f32_fp8_e32 v[216:217], v130
	v_cvt_pk_f32_fp8_e32 v[220:221], v134
	v_pk_fma_f32 v[188:189], s[40:41], v[188:189], 0 op_sel_hi:[0,1,0]
	v_cvt_pk_f32_fp8_e32 v[224:225], v138
	v_pk_fma_f32 v[188:189], s[38:39], v[196:197], v[188:189] op_sel_hi:[0,1,1]
	v_cvt_pk_f32_fp8_e32 v[196:197], v123
	v_cvt_pk_f32_fp8_sdwa v[198:199], v123 src0_sel:WORD_1
	s_waitcnt lgkmcnt(0)
; #define GAS __attribute__((address_space(1)))
; template <int l>
; __device__ __forceinline__ void layer_phases(Frame& F, const XcdBarrier& bar, const int lo, const int hi) {
;     ...
;                 for (int jh = 0; jh < 2; ++jh) {
; #pragma unroll
;                     for (int i = 0; i < 4; ++i) { const int j = 4 * jh + i, k = 16 * ln + 1024 * jh + 4 * i; f32x4 f = (f32x4){0.f, 0.f, 0.f, 0.f};
; #pragma unroll
;                         for (int q = 0; q < 7; ++q) { const unsigned w = yr[7 * jh + q][i]; const float gq = gt[q];
;                             const auto lo2 = __builtin_amdgcn_cvt_pk_f32_fp8((int)w, false), hi2 = __builtin_amdgcn_cvt_pk_f32_fp8((int)w, true);
;                             f.x += gq * lo2[0]; f.y += gq * lo2[1]; f.z += gq * hi2[0]; f.w += gq * hi2[1]; }
;                         v[j] = v[j] * ALPHA + *(const GAS f32x4*)(mrow + 10240 + k) * (f * (1.0f / (float)(1 << YSHIFT)));
;                         s += (v[j].x + v[j].y) + (v[j].z + v[j].w); }
;                 }
;                 const float mean = wave_sum(s) * (1.f / D); float s2 = 0.f;
; #pragma unroll
;                 for (int j = 0; j < 8; ++j) { v[j] = v[j] - mean; s2 += (v[j].x * v[j].x + v[j].y * v[j].y) + (v[j].z * v[j].z + v[j].w * v[j].w); }
	v_pk_mul_f32 v[192:193], v[192:193], v[194:195]
	v_cvt_pk_f32_fp8_sdwa v[194:195], v119 src0_sel:WORD_1
	v_pk_fma_f32 v[178:179], v[178:179], s[24:25], v[192:193] op_sel_hi:[1,0,1]
	v_cvt_pk_f32_fp8_e32 v[192:193], v119
	v_cvt_pk_f32_fp8_e32 v[228:229], v142
	v_pk_fma_f32 v[188:189], s[36:37], v[212:213], v[188:189] op_sel_hi:[0,1,1]
	v_cvt_pk_f32_fp8_e32 v[212:213], v127
	v_cvt_pk_f32_fp8_sdwa v[214:215], v127 src0_sel:WORD_1
	v_pk_fma_f32 v[188:189], s[34:35], v[216:217], v[188:189] op_sel_hi:[0,1,1]
	v_cvt_pk_f32_fp8_e32 v[216:217], v131
	v_cvt_pk_f32_fp8_sdwa v[218:219], v131 src0_sel:WORD_1
	v_pk_fma_f32 v[188:189], s[30:31], v[220:221], v[188:189] op_sel_hi:[0,1,1]
	v_cvt_pk_f32_fp8_e32 v[220:221], v135
	v_cvt_pk_f32_fp8_sdwa v[222:223], v135 src0_sel:WORD_1
	v_pk_fma_f32 v[194:195], s[40:41], v[194:195], 0 op_sel_hi:[0,1,0]
	v_pk_fma_f32 v[192:193], s[40:41], v[192:193], 0 op_sel_hi:[0,1,0]
	v_pk_fma_f32 v[188:189], s[0:1], v[224:225], v[188:189] op_sel_hi:[0,1,1]
	v_cvt_pk_f32_fp8_e32 v[224:225], v139
	v_cvt_pk_f32_fp8_sdwa v[226:227], v139 src0_sel:WORD_1
	v_pk_fma_f32 v[192:193], s[38:39], v[196:197], v[192:193] op_sel_hi:[0,1,1]
	v_pk_fma_f32 v[194:195], s[38:39], v[198:199], v[194:195] op_sel_hi:[0,1,1]
	v_pk_add_f32 v[188:189], v[188:189], v[228:229]
	v_cvt_pk_f32_fp8_e32 v[228:229], v143
	v_cvt_pk_f32_fp8_sdwa v[230:231], v143 src0_sel:WORD_1
	v_pk_fma_f32 v[194:195], s[36:37], v[214:215], v[194:195] op_sel_hi:[0,1,1]
	v_pk_fma_f32 v[192:193], s[36:37], v[212:213], v[192:193] op_sel_hi:[0,1,1]
	v_pk_fma_f32 v[192:193], s[34:35], v[216:217], v[192:193] op_sel_hi:[0,1,1]
	v_pk_fma_f32 v[194:195], s[34:35], v[218:219], v[194:195] op_sel_hi:[0,1,1]
	v_pk_fma_f32 v[194:195], s[30:31], v[222:223], v[194:195] op_sel_hi:[0,1,1]
	v_pk_fma_f32 v[192:193], s[30:31], v[220:221], v[192:193] op_sel_hi:[0,1,1]
	v_pk_fma_f32 v[192:193], s[0:1], v[224:225], v[192:193] op_sel_hi:[0,1,1]
	v_pk_fma_f32 v[194:195], s[0:1], v[226:227], v[194:195] op_sel_hi:[0,1,1]
	v_pk_add_f32 v[194:195], v[194:195], v[230:231]
	v_pk_add_f32 v[192:193], v[192:193], v[228:229]
	v_pk_mul_f32 v[188:189], v[188:189], s[22:23] op_sel_hi:[1,0]
	v_pk_mul_f32 v[192:193], v[192:193], s[22:23] op_sel_hi:[1,0]
	v_pk_mul_f32 v[194:195], v[194:195], s[22:23] op_sel_hi:[1,0]
	v_and_b32_e32 v167, 0xffff0000, v87
	v_pk_mul_f32 v[188:189], v[190:191], v[188:189]
	v_pk_mul_f32 v[182:183], v[182:183], v[194:195]
	v_pk_mul_f32 v[180:181], v[180:181], v[192:193]
	v_pk_add_f32 v[184:185], v[184:185], v[184:185] op_sel:[0,1] op_sel_hi:[1,0]
	v_pk_add_f32 v[186:187], v[186:187], v[186:187] op_sel:[0,1] op_sel_hi:[1,0]
	v_pk_fma_f32 v[172:173], v[172:173], s[24:25], v[188:189] op_sel_hi:[1,0,1]
	v_pk_fma_f32 v[166:167], v[166:167], s[24:25], v[182:183] op_sel_hi:[1,0,1]
	v_pk_fma_f32 v[164:165], v[164:165], s[24:25], v[180:181] op_sel_hi:[1,0,1]
	v_add_f32_e32 v188, v172, v173
	v_add_f32_e32 v190, v178, v179
	v_mov_b32_e32 v185, v164
	v_mov_b32_e32 v187, v165
	v_mov_b32_e32 v189, v166
	v_mov_b32_e32 v191, v167
	v_pk_add_f32 v[180:181], v[184:185], v[186:187]
	v_pk_add_f32 v[182:183], v[188:189], v[190:191]
	v_lshl_add_u64 v[188:189], s[8:9], 0, v[162:163]
	v_pk_add_f32 v[180:181], v[180:181], v[182:183]
	v_lshl_add_u64 v[190:191], s[10:11], 0, v[162:163]
	v_add_f32_e32 v161, v180, v181
	ds_bpermute_b32 v180, v203, v161
	s_ashr_i32 s29, s28, 31
	s_waitcnt lgkmcnt(0)
	v_add_f32_e32 v161, v161, v180
	ds_bpermute_b32 v180, v204, v161
	s_waitcnt lgkmcnt(0)
	v_add_f32_e32 v161, v161, v180
	ds_bpermute_b32 v180, v205, v161
	s_waitcnt lgkmcnt(0)
	v_add_f32_e32 v161, v161, v180
	ds_bpermute_b32 v180, v206, v161
	s_waitcnt lgkmcnt(0)
	v_add_f32_e32 v161, v161, v180
	ds_bpermute_b32 v180, v207, v161
	s_waitcnt lgkmcnt(0)
	v_add_f32_e32 v161, v161, v180
	ds_bpermute_b32 v180, v208, v161
	s_waitcnt lgkmcnt(0)
	v_add_f32_e32 v161, v161, v180
	v_fmamk_f32 v159, v161, 0xba000000, v159
	v_fmamk_f32 v155, v161, 0xba000000, v155
	v_fmamk_f32 v157, v161, 0xba000000, v157
	v_fmac_f32_e32 v158, 0xba000000, v161
	v_fmamk_f32 v153, v161, 0xba000000, v153
	v_fmac_f32_e32 v154, 0xba000000, v161
	v_mov_b32_e32 v182, v159
	v_mov_b32_e32 v183, v155
	v_fmac_f32_e32 v156, 0xba000000, v161
	v_fmac_f32_e32 v152, 0xba000000, v161
	v_mov_b32_e32 v180, v158
	v_mov_b32_e32 v181, v154
	v_pk_mul_f32 v[182:183], v[182:183], v[182:183]
	v_mov_b32_e32 v184, v157
	v_mov_b32_e32 v185, v153
	v_pk_fma_f32 v[180:181], v[180:181], v[180:181], v[182:183]
	v_mov_b32_e32 v182, v156
	v_mov_b32_e32 v183, v152
	v_pk_mul_f32 v[184:185], v[184:185], v[184:185]
	v_fmamk_f32 v149, v161, 0xba000000, v149
	v_pk_fma_f32 v[182:183], v[182:183], v[182:183], v[184:185]
	v_fmac_f32_e32 v148, 0xba000000, v161
	v_pk_add_f32 v[180:181], v[180:181], v[182:183]
	v_fmamk_f32 v151, v161, 0xba000000, v151
	v_fmac_f32_e32 v150, 0xba000000, v161
	v_pk_add_f32 v[180:181], v[180:181], v[180:181] op_sel_hi:[0,1]
	v_pk_mul_f32 v[182:183], v[150:151], v[150:151]
	v_pk_mul_f32 v[184:185], v[148:149], v[148:149]
	v_fmac_f32_e32 v144, 0xba000000, v161
	v_pk_mov_b32 v[186:187], v[184:185], v[182:183] op_sel:[1,0]
	v_mov_b32_e32 v185, v183
	v_fmamk_f32 v145, v161, 0xba000000, v145
	v_fmac_f32_e32 v146, 0xba000000, v161
	v_mul_f32_e32 v180, v144, v144
	v_pk_add_f32 v[182:183], v[186:187], v[184:185]
	v_fmamk_f32 v147, v161, 0xba000000, v147
	v_pk_fma_f32 v[184:185], v[144:145], v[144:145], v[180:181] op_sel_hi:[1,1,0]
	v_mul_f32_e32 v180, v146, v146
	v_pk_add_f32 v[182:183], v[182:183], v[182:183] op_sel_hi:[0,1]
	v_pk_fma_f32 v[186:187], v[146:147], v[146:147], v[180:181] op_sel_hi:[1,1,0]
	v_fmamk_f32 v169, v161, 0xba000000, v169
	v_fmac_f32_e32 v168, 0xba000000, v161
; #define GAS __attribute__((address_space(1)))
; template <int l>
; __device__ __forceinline__ void layer_phases(Frame& F, const XcdBarrier& bar, const int lo, const int hi) {
;     ...
;                 const float mean = wave_sum(s) * (1.f / D); float s2 = 0.f;
; #pragma unroll
;                 for (int j = 0; j < 8; ++j) { v[j] = v[j] - mean; s2 += (v[j].x * v[j].x + v[j].y * v[j].y) + (v[j].z * v[j].z + v[j].w * v[j].w); }
;                 const float rstd = 1.f / sqrtf(wave_sum(s2) * (1.f / D) + LN_EPS);
;                 float* orow = Fout + (size_t)m * D;
; #pragma unroll
;                 for (int j = 0; j < 8; ++j) { const int k = 16 * ln + 1024 * (j >> 2) + 4 * (j & 3);
;                     v[j] = v[j] * rstd * *(const GAS f32x4*)(g2 + k) + *(const GAS f32x4*)(b2 + k);
;                     if (l == 1) { *(GAS f32x4*)(orow + k) = v[j]; if (j & 1) asm volatile("" ::: "memory"); } }
	v_fmamk_f32 v171, v161, 0xba000000, v171
	v_fmac_f32_e32 v170, 0xba000000, v161
	v_mul_f32_e32 v184, v170, v170
	v_mul_f32_e32 v186, v171, v171
	v_mul_f32_e32 v182, v168, v168
	v_mul_f32_e32 v180, v169, v169
	v_pk_add_f32 v[184:185], v[184:185], v[186:187]
	v_pk_add_f32 v[180:181], v[182:183], v[180:181]
	v_fmamk_f32 v177, v161, 0xba000000, v177
	v_pk_add_f32 v[180:181], v[184:185], v[180:181]
	v_fmac_f32_e32 v176, 0xba000000, v161
	v_fmamk_f32 v175, v161, 0xba000000, v175
	v_fmac_f32_e32 v174, 0xba000000, v161
	v_pk_add_f32 v[180:181], v[180:181], v[180:181] op_sel_hi:[0,1]
	v_pk_mul_f32 v[182:183], v[174:175], v[174:175]
	v_pk_mul_f32 v[184:185], v[176:177], v[176:177]
	v_fmac_f32_e32 v172, 0xba000000, v161
	v_pk_mov_b32 v[186:187], v[184:185], v[182:183] op_sel:[1,0]
	v_mov_b32_e32 v185, v183
	v_fmamk_f32 v173, v161, 0xba000000, v173
	v_fmac_f32_e32 v178, 0xba000000, v161
	v_mul_f32_e32 v180, v172, v172
	v_pk_add_f32 v[182:183], v[186:187], v[184:185]
	v_fmamk_f32 v179, v161, 0xba000000, v179
	v_pk_fma_f32 v[184:185], v[172:173], v[172:173], v[180:181] op_sel_hi:[1,1,0]
	v_mul_f32_e32 v180, v178, v178
	v_pk_add_f32 v[182:183], v[182:183], v[182:183] op_sel_hi:[0,1]
	v_pk_fma_f32 v[186:187], v[178:179], v[178:179], v[180:181] op_sel_hi:[1,1,0]
	v_fmamk_f32 v167, v161, 0xba000000, v167
	v_fmac_f32_e32 v166, 0xba000000, v161
	v_fmamk_f32 v165, v161, 0xba000000, v165
	v_fmac_f32_e32 v164, 0xba000000, v161
	v_mul_f32_e32 v184, v164, v164
	v_mul_f32_e32 v186, v165, v165
	v_mul_f32_e32 v182, v166, v166
	v_mul_f32_e32 v180, v167, v167
	v_pk_add_f32 v[184:185], v[184:185], v[186:187]
	v_pk_add_f32 v[180:181], v[182:183], v[180:181]
	s_nop 0
	v_pk_add_f32 v[180:181], v[184:185], v[180:181]
	v_add_u32_e32 v247, s99, v190
	ds_read_b128 v[184:187], v247
	v_add_f32_e32 v161, v180, v181
	v_add_u32_e32 v247, s98, v188
	ds_read_b128 v[180:183], v247
	ds_bpermute_b32 v192, v203, v161
	s_waitcnt lgkmcnt(0)
	v_add_f32_e32 v161, v161, v192
	ds_bpermute_b32 v192, v204, v161
	s_waitcnt lgkmcnt(0)
	v_add_f32_e32 v161, v161, v192
	ds_bpermute_b32 v192, v205, v161
	s_waitcnt lgkmcnt(0)
	v_add_f32_e32 v161, v161, v192
	ds_bpermute_b32 v192, v206, v161
	s_waitcnt lgkmcnt(0)
	v_add_f32_e32 v161, v161, v192
	ds_bpermute_b32 v192, v207, v161
	s_waitcnt lgkmcnt(0)
	v_add_f32_e32 v161, v161, v192
	ds_bpermute_b32 v192, v208, v161
	s_waitcnt lgkmcnt(0)
	v_add_f32_e32 v161, v161, v192
	v_fmamk_f32 v161, v161, 0x3a000000, v209
	v_mul_f32_e32 v192, 0x4f800000, v161
	v_cmp_gt_f32_e32 vcc, s55, v161
	s_nop 1
	v_cndmask_b32_e32 v161, v161, v192, vcc
	v_sqrt_f32_e32 v192, v161
	s_nop 0
	v_add_u32_e32 v193, -1, v192
	v_fma_f32 v194, -v193, v192, v161
	v_cmp_ge_f32_e64 s[0:1], 0, v194
	v_add_u32_e32 v194, 1, v192
	s_nop 0
	v_cndmask_b32_e64 v193, v192, v193, s[0:1]
	v_fma_f32 v192, -v194, v192, v161
	v_cmp_lt_f32_e64 s[0:1], 0, v192
	s_nop 1
	v_cndmask_b32_e64 v192, v193, v194, s[0:1]
	v_mul_f32_e32 v193, 0x37800000, v192
	v_cndmask_b32_e32 v192, v192, v193, vcc
	v_cmp_class_f32_e32 vcc, v161, v210
	s_nop 1
	v_cndmask_b32_e32 v161, v192, v161, vcc
	v_div_scale_f32 v192, s[0:1], v161, v161, 1.0
	v_rcp_f32_e32 v193, v192
	s_lshl_b64 s[0:1], s[28:29], 13
	s_add_u32 s0, s25, s0
	s_addc_u32 s1, s23, s1
	v_fma_f32 v194, -v192, v193, 1.0
	v_fmac_f32_e32 v193, v194, v193
	v_div_scale_f32 v194, vcc, 1.0, v161, 1.0
	v_mul_f32_e32 v195, v194, v193
	v_fma_f32 v196, -v192, v195, v194
	v_fmac_f32_e32 v195, v196, v193
	v_fma_f32 v192, -v192, v195, v194
	v_div_fmas_f32 v192, v192, v193, v195
	v_div_fixup_f32 v192, v192, v161, 1.0
	v_pk_mul_f32 v[194:195], v[158:159], v[192:193] op_sel_hi:[1,0]
	v_pk_mul_f32 v[156:157], v[156:157], v[192:193] op_sel_hi:[1,0]
	v_lshl_add_u64 v[162:163], s[0:1], 0, v[162:163]
	s_waitcnt lgkmcnt(0)
	v_pk_fma_f32 v[158:159], v[182:183], v[156:157], v[186:187]
	v_pk_fma_f32 v[156:157], v[180:181], v[194:195], v[184:185]
	global_store_dwordx4 v[162:163], v[156:159], off
	v_pk_mul_f32 v[184:185], v[152:153], v[192:193] op_sel_hi:[1,0]
	v_pk_mul_f32 v[152:153], v[154:155], v[192:193] op_sel_hi:[1,0]
	v_or_b32_e32 v156, 4, v160
	v_ashrrev_i32_e32 v157, 31, v156
	v_lshlrev_b64 v[180:181], 2, v[156:157]
	v_lshl_add_u64 v[156:157], s[8:9], 0, v[180:181]
	v_lshl_add_u64 v[180:181], s[10:11], 0, v[180:181]
	v_add_u32_e32 v247, s98, v156
	ds_read_b128 v[156:159], v247
	v_pk_mul_f32 v[150:151], v[150:151], v[192:193] op_sel_hi:[1,0]
	v_add_u32_e32 v247, s99, v180
	ds_read_b128 v[180:183], v247
	v_pk_mul_f32 v[148:149], v[148:149], v[192:193] op_sel_hi:[1,0]
	v_pk_mul_f32 v[146:147], v[146:147], v[192:193] op_sel_hi:[1,0]
	v_pk_mul_f32 v[144:145], v[144:145], v[192:193] op_sel_hi:[1,0]
	s_waitcnt lgkmcnt(0)
; #define GAS __attribute__((address_space(1)))
; template <int l>
; __device__ __forceinline__ void layer_phases(Frame& F, const XcdBarrier& bar, const int lo, const int hi) {
;     ...
; #pragma unroll
;                 for (int j = 0; j < 8; ++j) { const int k = 16 * ln + 1024 * (j >> 2) + 4 * (j & 3);
;                     v[j] = v[j] * rstd * *(const GAS f32x4*)(g2 + k) + *(const GAS f32x4*)(b2 + k);
;                     if (l == 1) { *(GAS f32x4*)(orow + k) = v[j]; if (j & 1) asm volatile("" ::: "memory"); } }
	v_pk_fma_f32 v[152:153], v[156:157], v[152:153], v[180:181]
	v_pk_fma_f32 v[154:155], v[158:159], v[184:185], v[182:183]
	global_store_dwordx4 v[162:163], v[152:155], off offset:16
	s_nop 1
	v_or_b32_e32 v152, 8, v160
	v_ashrrev_i32_e32 v153, 31, v152
	v_lshlrev_b64 v[156:157], 2, v[152:153]
	v_lshl_add_u64 v[152:153], s[8:9], 0, v[156:157]
	v_lshl_add_u64 v[156:157], s[10:11], 0, v[156:157]
	v_add_u32_e32 v247, s98, v152
	ds_read_b128 v[152:155], v247
	s_nop 0
	v_add_u32_e32 v247, s99, v156
	ds_read_b128 v[156:159], v247
	s_waitcnt lgkmcnt(0)
	v_pk_fma_f32 v[148:149], v[152:153], v[148:149], v[156:157]
	v_pk_fma_f32 v[150:151], v[154:155], v[150:151], v[158:159]
	global_store_dwordx4 v[162:163], v[148:151], off offset:32
	s_nop 1
	v_or_b32_e32 v148, 12, v160
	v_ashrrev_i32_e32 v149, 31, v148
	v_lshlrev_b64 v[152:153], 2, v[148:149]
	v_lshl_add_u64 v[148:149], s[8:9], 0, v[152:153]
	v_lshl_add_u64 v[152:153], s[10:11], 0, v[152:153]
	v_add_u32_e32 v247, s98, v148
	ds_read_b128 v[148:151], v247
	s_nop 0
	v_add_u32_e32 v247, s99, v152
	ds_read_b128 v[152:155], v247
	s_waitcnt lgkmcnt(0)
	v_pk_fma_f32 v[144:145], v[148:149], v[144:145], v[152:153]
	v_pk_fma_f32 v[146:147], v[150:151], v[146:147], v[154:155]
	global_store_dwordx4 v[162:163], v[144:147], off offset:48
	v_pk_mul_f32 v[154:155], v[170:171], v[192:193] op_sel_hi:[1,0]
	v_pk_mul_f32 v[152:153], v[168:169], v[192:193] op_sel_hi:[1,0]
	v_add_co_u32_e32 v144, vcc, s51, v188
	v_pk_mul_f32 v[168:169], v[176:177], v[192:193] op_sel_hi:[1,0]
	s_nop 0
	v_addc_co_u32_e32 v145, vcc, 0, v189, vcc
	v_add_co_u32_e32 v148, vcc, s51, v190
	v_add_u32_e32 v247, s98, v144
	ds_read_b128 v[144:147], v247
	s_nop 0
	v_addc_co_u32_e32 v149, vcc, 0, v191, vcc
	v_add_u32_e32 v247, s99, v148
	ds_read_b128 v[148:151], v247
	s_waitcnt lgkmcnt(0)
	v_pk_fma_f32 v[144:145], v[144:145], v[154:155], v[148:149]
	v_add_co_u32_e32 v148, vcc, s51, v162
	v_pk_fma_f32 v[146:147], v[146:147], v[152:153], v[150:151]
	s_nop 0
	v_addc_co_u32_e32 v149, vcc, 0, v163, vcc
	global_store_dwordx4 v[148:149], v[144:147], off
	v_add_u32_e32 v154, 0x408, v160
	v_pk_mul_f32 v[162:163], v[174:175], v[192:193] op_sel_hi:[1,0]
	v_add_u32_e32 v144, 0x404, v160
	v_ashrrev_i32_e32 v145, 31, v144
	v_lshlrev_b64 v[152:153], 2, v[144:145]
	v_lshl_add_u64 v[144:145], s[8:9], 0, v[152:153]
	v_lshl_add_u64 v[148:149], s[10:11], 0, v[152:153]
	v_add_u32_e32 v247, s98, v144
	ds_read_b128 v[144:147], v247
	v_ashrrev_i32_e32 v155, 31, v154
	v_add_u32_e32 v247, s99, v148
	ds_read_b128 v[148:151], v247
	v_lshl_add_u64 v[152:153], s[0:1], 0, v[152:153]
	v_lshlrev_b64 v[154:155], 2, v[154:155]
	v_lshl_add_u64 v[156:157], s[8:9], 0, v[154:155]
	v_lshl_add_u64 v[158:159], s[10:11], 0, v[154:155]
	v_lshl_add_u64 v[154:155], s[0:1], 0, v[154:155]
	s_waitcnt lgkmcnt(0)
	v_pk_fma_f32 v[144:145], v[144:145], v[168:169], v[148:149]
	v_pk_fma_f32 v[146:147], v[146:147], v[162:163], v[150:151]
	global_store_dwordx4 v[152:153], v[144:147], off
	v_add_u32_e32 v247, s98, v156
	ds_read_b128 v[144:147], v247
	v_add_u32_e32 v247, s99, v158
	ds_read_b128 v[148:151], v247
	v_add_u32_e32 v152, 0x40c, v160
	v_ashrrev_i32_e32 v153, 31, v152
	v_pk_mul_f32 v[160:161], v[178:179], v[192:193] op_sel_hi:[1,0]
	v_pk_mul_f32 v[162:163], v[172:173], v[192:193] op_sel_hi:[1,0]
	v_lshlrev_b64 v[152:153], 2, v[152:153]
	v_lshl_add_u64 v[156:157], s[8:9], 0, v[152:153]
	v_lshl_add_u64 v[158:159], s[10:11], 0, v[152:153]
	s_waitcnt lgkmcnt(0)
	v_pk_fma_f32 v[144:145], v[144:145], v[162:163], v[148:149]
	v_pk_fma_f32 v[146:147], v[146:147], v[160:161], v[150:151]
	global_store_dwordx4 v[154:155], v[144:147], off
	v_add_u32_e32 v247, s98, v156
	ds_read_b128 v[144:147], v247
	s_nop 0
	v_add_u32_e32 v247, s99, v158
	ds_read_b128 v[148:151], v247
	v_pk_mul_f32 v[154:155], v[166:167], v[192:193] op_sel_hi:[1,0]
	v_pk_mul_f32 v[156:157], v[164:165], v[192:193] op_sel_hi:[1,0]
	s_waitcnt lgkmcnt(0)
	v_pk_fma_f32 v[146:147], v[146:147], v[154:155], v[150:151]
	v_pk_fma_f32 v[144:145], v[144:145], v[156:157], v[148:149]
	v_lshl_add_u64 v[148:149], s[0:1], 0, v[152:153]
	global_store_dwordx4 v[148:149], v[144:147], off

; #define GAS __attribute__((address_space(1)))
; template <int l>
; __device__ __forceinline__ void layer_phases(Frame& F, const XcdBarrier& bar, const int lo, const int hi) {
;     ...
;             auto load_row = [&](const int m, v4u (&xr)[4], v4u (&yr)[14], float& gtv) {
;                 int ln = F.lane; asm volatile("" : "+v"(ln));
;                 gtv = 0.f; if (ln < 6) gtv = gates[(size_t)m * 6 + ln];
; #pragma unroll
;                 for (int jh = 0; jh < 2; ++jh) { xr[2 * jh] = __builtin_nontemporal_load((const GAS v4u*)(x1 + (size_t)m * D + 16 * ln + 1024 * jh)); xr[2 * jh + 1] = __builtin_nontemporal_load((const GAS v4u*)(x1 + (size_t)m * D + 16 * ln + 1024 * jh + 8)); }
; #pragma unroll
;                 for (int jh = 0; jh < 2; ++jh)
; #pragma unroll
;                     for (int q = 0; q < 7; ++q) yr[7 * jh + q] = __builtin_nontemporal_load((const GAS v4u*)(yb + ((size_t)m * 7 + q) * D + 16 * ln + 1024 * jh));
;                 asm volatile("" ::: "memory");
;     ...
;                     if (hasB) load_row(row_of(m_ + NGW), xB, yB, gB);
.LBB0_1886:
	s_or_b64 exec, exec, s[34:35]
	s_lshl_b64 s[34:35], s[2:3], 12
	s_add_u32 s34, s48, s34
	s_addc_u32 s35, s49, s35
	s_mul_hi_i32 s3, s2, 0x3800
	s_mulk_i32 s2, 0x3800
	v_lshlrev_b32_e32 v88, 4, v68
	s_add_u32 s2, s46, s2
	v_ashrrev_i32_e32 v89, 31, v88
	s_addc_u32 s3, s47, s3
	v_lshl_add_u64 v[112:113], s[2:3], 0, v[88:89]
	v_add_co_u32_e32 v114, vcc, s51, v112
	v_lshl_add_u64 v[90:91], v[88:89], 1, s[34:35]
	s_nop 0
	v_addc_co_u32_e32 v115, vcc, 0, v113, vcc
	v_add_co_u32_e32 v96, vcc, s52, v112
	v_lshl_add_u64 v[124:125], v[112:113], 0, s[12:13]
	s_nop 0
	v_addc_co_u32_e32 v97, vcc, 0, v113, vcc
	v_add_co_u32_e32 v100, vcc, 0x3000, v112
	v_lshl_add_u64 v[128:129], v[112:113], 0, s[14:15]
	v_lshl_add_u64 v[132:133], v[112:113], 0, s[6:7]
	v_lshl_add_u64 v[136:137], v[112:113], 0, s[16:17]
	v_lshl_add_u64 v[140:141], v[112:113], 0, s[18:19]
	v_addc_co_u32_e32 v101, vcc, 0, v113, vcc
	global_load_dwordx4 v[72:75], v[90:91], off offset:16 nt
	global_load_dwordx4 v[68:71], v[90:91], off nt
	global_load_dwordx4 v[84:87], v[90:91], off offset:2064 nt
	global_load_dwordx4 v[80:83], v[90:91], off offset:2048 nt
	s_nop 0
	global_load_dwordx4 v[88:91], v[96:97], off nt
	global_load_dwordx4 v[92:95], v[96:97], off offset:2048 nt
	s_nop 0
	global_load_dwordx4 v[96:99], v[96:97], off offset:-4096 nt
	s_nop 0
	global_load_dwordx4 v[108:111], v[100:101], off nt
	s_nop 0
	global_load_dwordx4 v[100:103], v[112:113], off nt
	global_load_dwordx4 v[116:119], v[112:113], off offset:1024 nt
	global_load_dwordx4 v[104:107], v[112:113], off offset:2048 nt
	global_load_dwordx4 v[120:123], v[112:113], off offset:3072 nt
	s_nop 0
	global_load_dwordx4 v[112:115], v[114:115], off offset:2048 nt
	s_nop 0
	global_load_dwordx4 v[124:127], v[124:125], off offset:1024 nt
	s_nop 0
	global_load_dwordx4 v[128:131], v[128:129], off offset:1024 nt
	s_nop 0
	global_load_dwordx4 v[132:135], v[132:133], off offset:1024 nt
	s_nop 0
	global_load_dwordx4 v[136:139], v[136:137], off offset:1024 nt
	s_nop 0
	global_load_dwordx4 v[140:143], v[140:141], off offset:1024 nt
	s_waitcnt vmcnt(19)

; #define GAS __attribute__((address_space(1)))
; __device__ __forceinline__ f32x4 bf4(unsigned a, unsigned b) { return (f32x4){bflo(a), bfhi(a), bflo(b), bfhi(b)}; }
; template <int l>
; __device__ __forceinline__ void layer_phases(Frame& F, const XcdBarrier& bar, const int lo, const int hi) {
;     ...
;             auto process_row = [&](const int m, v4u (&xr)[4], v4u (&yr)[14], const float gtv) {
;                 int ln = F.lane; asm volatile("" : "+v"(ln));
;                 const float* mrow = (const float*)(ws + WS_MOD) + ((size_t)l * 8 + (m >> 11)) * 12288;
;                 float gt[7];
; #pragma unroll
;                 for (int k = 0; k < 6; ++k) gt[k] = __uint_as_float((unsigned)__builtin_amdgcn_readlane((int)__float_as_uint(gtv), k));
;                 gt[6] = 1.0f;
;                 f32x4 v[8]; float s = 0.f;
; #pragma unroll
;                 for (int jh = 0; jh < 2; ++jh) { const v4u xa = xr[2 * jh], xb = xr[2 * jh + 1];
;                     v[4 * jh] = bf4(xa.x, xa.y); v[4 * jh + 1] = bf4(xa.z, xa.w); v[4 * jh + 2] = bf4(xb.x, xb.y); v[4 * jh + 3] = bf4(xb.z, xb.w); }
; #pragma unroll
;                 for (int jh = 0; jh < 2; ++jh) {
; #pragma unroll
;                     for (int i = 0; i < 4; ++i) { const int j = 4 * jh + i, k = 16 * ln + 1024 * jh + 4 * i; f32x4 f = (f32x4){0.f, 0.f, 0.f, 0.f};
; #pragma unroll
;                         for (int q = 0; q < 7; ++q) { const unsigned w = yr[7 * jh + q][i]; const float gq = gt[q];
;                             const auto lo2 = __builtin_amdgcn_cvt_pk_f32_fp8((int)w, false), hi2 = __builtin_amdgcn_cvt_pk_f32_fp8((int)w, true);
;                             f.x += gq * lo2[0]; f.y += gq * lo2[1]; f.z += gq * hi2[0]; f.w += gq * hi2[1]; }
;                         v[j] = v[j] * ALPHA + *(const GAS f32x4*)(mrow + 10240 + k) * (f * (1.0f / (float)(1 << YSHIFT)));
.LBB0_1889:
	s_ashr_i32 s2, s34, 11
	s_lshl_b32 s100, s2, 13
	v_mov_b32_e32 v144, v200
	s_add_i32 s2, s2, 8
	s_mul_hi_i32 s3, s2, 0xc000
	s_mul_i32 s2, s2, 0xc000
	v_lshlrev_b32_e32 v160, 4, v144
	s_add_u32 s2, s56, s2
	v_ashrrev_i32_e32 v161, 31, v160
	s_addc_u32 s3, s57, s3
	s_sub_u32 s100, s100, s2
	s_sub_u32 s100, s100, 0x10a000
	v_lshlrev_b64 v[162:163], 2, v[160:161]
	v_lshl_add_u64 v[180:181], s[2:3], 0, v[162:163]
	v_add_co_u32_e32 v194, vcc, s54, v180
	v_lshl_add_u64 v[144:145], v[180:181], 0, s[20:21]
	s_nop 0
	v_addc_co_u32_e32 v195, vcc, 0, v181, vcc
	v_add_u32_e32 v247, s100, v194
	v_add_u32_e32 v247, 0xfffff000, v247
	ds_read_b128 v[156:159], v247
	v_add_u32_e32 v247, s100, v144
	ds_read_b128 v[148:151], v247 offset:32
	v_add_u32_e32 v247, s100, v144
	ds_read_b128 v[152:155], v247 offset:16
	s_waitcnt lgkmcnt(0)
	v_cvt_pk_f32_fp8_e32 v[146:147], v32
	s_waitcnt lgkmcnt(0)
	v_cvt_pk_f32_fp8_e32 v[214:215], v40
	v_cvt_pk_f32_fp8_e32 v[218:219], v24
	v_readlane_b32 s44, v202, 0
	s_waitcnt lgkmcnt(0)
	v_cvt_pk_f32_fp8_e32 v[222:223], v48
	v_readlane_b32 s42, v202, 1
	v_cvt_pk_f32_fp8_e32 v[226:227], v16
	v_pk_fma_f32 v[146:147], s[44:45], v[146:147], 0 op_sel_hi:[0,1,0]
	v_readlane_b32 s40, v202, 2
	v_cvt_pk_f32_fp8_e32 v[230:231], v20
	v_pk_fma_f32 v[146:147], s[42:43], v[214:215], v[146:147] op_sel_hi:[0,1,1]
	v_readlane_b32 s38, v202, 3
	v_cvt_pk_f32_fp8_e32 v[234:235], v28
	v_pk_fma_f32 v[146:147], s[40:41], v[218:219], v[146:147] op_sel_hi:[0,1,1]
	v_readlane_b32 s36, v202, 4
	v_pk_fma_f32 v[146:147], s[38:39], v[222:223], v[146:147] op_sel_hi:[0,1,1]
	v_readlane_b32 s2, v202, 5
	v_pk_fma_f32 v[146:147], s[36:37], v[226:227], v[146:147] op_sel_hi:[0,1,1]
	v_cvt_pk_f32_fp8_sdwa v[212:213], v32 src0_sel:WORD_1
	v_pk_fma_f32 v[146:147], s[2:3], v[230:231], v[146:147] op_sel_hi:[0,1,1]
	v_pk_add_f32 v[214:215], v[146:147], v[234:235]
	v_add_u32_e32 v247, s100, v144
	ds_read_b128 v[144:147], v247 offset:48
	v_cvt_pk_f32_fp8_sdwa v[216:217], v40 src0_sel:WORD_1
	v_cvt_pk_f32_fp8_sdwa v[220:221], v24 src0_sel:WORD_1
	v_cvt_pk_f32_fp8_sdwa v[224:225], v48 src0_sel:WORD_1
	v_cvt_pk_f32_fp8_sdwa v[228:229], v16 src0_sel:WORD_1
	v_pk_fma_f32 v[212:213], s[44:45], v[212:213], 0 op_sel_hi:[0,1,0]
	v_cvt_pk_f32_fp8_sdwa v[232:233], v20 src0_sel:WORD_1
	v_pk_fma_f32 v[212:213], s[42:43], v[216:217], v[212:213] op_sel_hi:[0,1,1]
	v_cvt_pk_f32_fp8_sdwa v[236:237], v28 src0_sel:WORD_1
	v_pk_fma_f32 v[212:213], s[40:41], v[220:221], v[212:213] op_sel_hi:[0,1,1]
	v_pk_fma_f32 v[212:213], s[38:39], v[224:225], v[212:213] op_sel_hi:[0,1,1]
	v_pk_fma_f32 v[212:213], s[36:37], v[228:229], v[212:213] op_sel_hi:[0,1,1]
	v_pk_fma_f32 v[212:213], s[2:3], v[232:233], v[212:213] op_sel_hi:[0,1,1]
	v_pk_add_f32 v[212:213], v[212:213], v[236:237]
	v_pk_mul_f32 v[216:217], v[214:215], s[22:23] op_sel_hi:[1,0]
	v_pk_mul_f32 v[218:219], v[212:213], s[22:23] op_sel_hi:[1,0]
	v_lshlrev_b32_e32 v196, 16, v4
	v_and_b32_e32 v197, 0xffff0000, v4
	v_lshlrev_b32_e32 v198, 16, v5
	v_and_b32_e32 v199, 0xffff0000, v5
	v_add_u32_e32 v247, s100, v194
	ds_read_b128 v[212:215], v247
	v_cvt_pk_f32_fp8_sdwa v[220:221], v25 src0_sel:WORD_1
	v_cvt_pk_f32_fp8_e32 v[222:223], v49
	v_cvt_pk_f32_fp8_sdwa v[224:225], v49 src0_sel:WORD_1
	v_cvt_pk_f32_fp8_e32 v[226:227], v17
	v_cvt_pk_f32_fp8_sdwa v[228:229], v17 src0_sel:WORD_1
	v_cvt_pk_f32_fp8_e32 v[230:231], v21
	v_cvt_pk_f32_fp8_sdwa v[232:233], v21 src0_sel:WORD_1
	v_cvt_pk_f32_fp8_e32 v[234:235], v29
	v_cvt_pk_f32_fp8_sdwa v[236:237], v29 src0_sel:WORD_1
	v_lshlrev_b32_e32 v190, 16, v6
	v_and_b32_e32 v191, 0xffff0000, v6
	v_lshlrev_b32_e32 v192, 16, v7
	v_and_b32_e32 v193, 0xffff0000, v7
	v_lshlrev_b32_e32 v186, 16, v0
	v_and_b32_e32 v187, 0xffff0000, v0
	v_lshlrev_b32_e32 v188, 16, v1
	v_and_b32_e32 v189, 0xffff0000, v1
	v_lshlrev_b32_e32 v182, 16, v2
	v_and_b32_e32 v183, 0xffff0000, v2
	v_lshlrev_b32_e32 v184, 16, v3
	v_and_b32_e32 v185, 0xffff0000, v3
	v_lshlrev_b32_e32 v170, 16, v12
	v_and_b32_e32 v171, 0xffff0000, v12
	v_lshlrev_b32_e32 v168, 16, v13
	v_and_b32_e32 v169, 0xffff0000, v13
	v_lshlrev_b32_e32 v176, 16, v14
	v_and_b32_e32 v177, 0xffff0000, v14
	v_lshlrev_b32_e32 v174, 16, v15
	v_and_b32_e32 v175, 0xffff0000, v15
	v_lshlrev_b32_e32 v178, 16, v9
	v_and_b32_e32 v179, 0xffff0000, v9
	v_lshlrev_b32_e32 v172, 16, v8
	v_and_b32_e32 v173, 0xffff0000, v8
	v_lshlrev_b32_e32 v164, 16, v10
	v_and_b32_e32 v165, 0xffff0000, v10
	v_lshlrev_b32_e32 v166, 16, v11
	s_waitcnt lgkmcnt(0)
	v_pk_mul_f32 v[158:159], v[158:159], v[218:219]
	v_pk_mul_f32 v[194:195], v[156:157], v[216:217]
	v_pk_fma_f32 v[156:157], v[198:199], s[24:25], v[158:159] op_sel_hi:[1,0,1]
	v_pk_fma_f32 v[158:159], v[196:197], s[24:25], v[194:195] op_sel_hi:[1,0,1]
	v_cvt_pk_f32_fp8_e32 v[194:195], v33
	v_cvt_pk_f32_fp8_sdwa v[196:197], v33 src0_sel:WORD_1
	v_cvt_pk_f32_fp8_e32 v[198:199], v41
	v_cvt_pk_f32_fp8_sdwa v[216:217], v41 src0_sel:WORD_1
	v_cvt_pk_f32_fp8_e32 v[218:219], v25
	v_pk_fma_f32 v[196:197], s[44:45], v[196:197], 0 op_sel_hi:[0,1,0]
	v_pk_fma_f32 v[194:195], s[44:45], v[194:195], 0 op_sel_hi:[0,1,0]
	v_pk_fma_f32 v[194:195], s[42:43], v[198:199], v[194:195] op_sel_hi:[0,1,1]
	v_pk_fma_f32 v[196:197], s[42:43], v[216:217], v[196:197] op_sel_hi:[0,1,1]
	v_pk_fma_f32 v[196:197], s[40:41], v[220:221], v[196:197] op_sel_hi:[0,1,1]
	v_pk_fma_f32 v[194:195], s[40:41], v[218:219], v[194:195] op_sel_hi:[0,1,1]
	v_pk_fma_f32 v[194:195], s[38:39], v[222:223], v[194:195] op_sel_hi:[0,1,1]
	v_pk_fma_f32 v[196:197], s[38:39], v[224:225], v[196:197] op_sel_hi:[0,1,1]
	v_pk_fma_f32 v[196:197], s[36:37], v[228:229], v[196:197] op_sel_hi:[0,1,1]
	v_pk_fma_f32 v[194:195], s[36:37], v[226:227], v[194:195] op_sel_hi:[0,1,1]
	v_pk_fma_f32 v[194:195], s[2:3], v[230:231], v[194:195] op_sel_hi:[0,1,1]
	v_pk_fma_f32 v[196:197], s[2:3], v[232:233], v[196:197] op_sel_hi:[0,1,1]
	v_pk_add_f32 v[196:197], v[196:197], v[236:237]
	v_pk_add_f32 v[194:195], v[194:195], v[234:235]
	v_pk_mul_f32 v[196:197], v[196:197], s[22:23] op_sel_hi:[1,0]
	v_pk_mul_f32 v[194:195], v[194:195], s[22:23] op_sel_hi:[1,0]
	s_waitcnt lgkmcnt(0)
; #define GAS __attribute__((address_space(1)))
; template <int l>
; __device__ __forceinline__ void layer_phases(Frame& F, const XcdBarrier& bar, const int lo, const int hi) {
;     ...
;                 for (int jh = 0; jh < 2; ++jh) {
; #pragma unroll
;                     for (int i = 0; i < 4; ++i) { const int j = 4 * jh + i, k = 16 * ln + 1024 * jh + 4 * i; f32x4 f = (f32x4){0.f, 0.f, 0.f, 0.f};
; #pragma unroll
;                         for (int q = 0; q < 7; ++q) { const unsigned w = yr[7 * jh + q][i]; const float gq = gt[q];
;                             const auto lo2 = __builtin_amdgcn_cvt_pk_f32_fp8((int)w, false), hi2 = __builtin_amdgcn_cvt_pk_f32_fp8((int)w, true);
;                             f.x += gq * lo2[0]; f.y += gq * lo2[1]; f.z += gq * hi2[0]; f.w += gq * hi2[1]; }
;                         v[j] = v[j] * ALPHA + *(const GAS f32x4*)(mrow + 10240 + k) * (f * (1.0f / (float)(1 << YSHIFT)));
;                         s += (v[j].x + v[j].y) + (v[j].z + v[j].w); }
	v_pk_mul_f32 v[154:155], v[154:155], v[196:197]
	v_pk_mul_f32 v[194:195], v[152:153], v[194:195]
	v_pk_fma_f32 v[152:153], v[192:193], s[24:25], v[154:155] op_sel_hi:[1,0,1]
	v_pk_fma_f32 v[154:155], v[190:191], s[24:25], v[194:195] op_sel_hi:[1,0,1]
	v_mov_b32_e32 v190, v158
	v_mov_b32_e32 v191, v154
	v_mov_b32_e32 v192, v159
	v_mov_b32_e32 v193, v155
	v_pk_add_f32 v[190:191], v[190:191], v[192:193]
	v_mov_b32_e32 v192, v156
	v_mov_b32_e32 v193, v152
	v_mov_b32_e32 v194, v157
	v_mov_b32_e32 v195, v153
	v_pk_add_f32 v[192:193], v[192:193], v[194:195]
	v_cvt_pk_f32_fp8_e32 v[196:197], v42
	v_pk_add_f32 v[190:191], v[190:191], v[192:193]
	v_cvt_pk_f32_fp8_sdwa v[192:193], v34 src0_sel:WORD_1
	v_add_f32_e32 v161, 0, v190
	v_add_f32_e32 v194, v161, v191
	v_cvt_pk_f32_fp8_e32 v[190:191], v34
	v_cvt_pk_f32_fp8_sdwa v[198:199], v42 src0_sel:WORD_1
	v_cvt_pk_f32_fp8_e32 v[216:217], v26
	v_cvt_pk_f32_fp8_sdwa v[218:219], v26 src0_sel:WORD_1
	v_cvt_pk_f32_fp8_e32 v[220:221], v50
	v_cvt_pk_f32_fp8_sdwa v[222:223], v50 src0_sel:WORD_1
	v_cvt_pk_f32_fp8_e32 v[224:225], v18
	v_cvt_pk_f32_fp8_sdwa v[226:227], v18 src0_sel:WORD_1
	v_pk_fma_f32 v[192:193], s[44:45], v[192:193], 0 op_sel_hi:[0,1,0]
	v_pk_fma_f32 v[190:191], s[44:45], v[190:191], 0 op_sel_hi:[0,1,0]
	v_cvt_pk_f32_fp8_e32 v[228:229], v22
	v_cvt_pk_f32_fp8_sdwa v[230:231], v22 src0_sel:WORD_1
	v_pk_fma_f32 v[190:191], s[42:43], v[196:197], v[190:191] op_sel_hi:[0,1,1]
	v_pk_fma_f32 v[192:193], s[42:43], v[198:199], v[192:193] op_sel_hi:[0,1,1]
	v_cvt_pk_f32_fp8_e32 v[232:233], v30
	v_cvt_pk_f32_fp8_sdwa v[234:235], v30 src0_sel:WORD_1
	v_pk_fma_f32 v[192:193], s[40:41], v[218:219], v[192:193] op_sel_hi:[0,1,1]
	v_pk_fma_f32 v[190:191], s[40:41], v[216:217], v[190:191] op_sel_hi:[0,1,1]
	v_pk_fma_f32 v[190:191], s[38:39], v[220:221], v[190:191] op_sel_hi:[0,1,1]
	v_pk_fma_f32 v[192:193], s[38:39], v[222:223], v[192:193] op_sel_hi:[0,1,1]
	v_pk_fma_f32 v[192:193], s[36:37], v[226:227], v[192:193] op_sel_hi:[0,1,1]
	v_pk_fma_f32 v[190:191], s[36:37], v[224:225], v[190:191] op_sel_hi:[0,1,1]
	v_pk_fma_f32 v[190:191], s[2:3], v[228:229], v[190:191] op_sel_hi:[0,1,1]
	v_pk_fma_f32 v[192:193], s[2:3], v[230:231], v[192:193] op_sel_hi:[0,1,1]
	v_pk_add_f32 v[192:193], v[192:193], v[234:235]
	v_pk_add_f32 v[190:191], v[190:191], v[232:233]
	v_pk_mul_f32 v[192:193], v[192:193], s[22:23] op_sel_hi:[1,0]
	v_pk_mul_f32 v[190:191], v[190:191], s[22:23] op_sel_hi:[1,0]
	v_pk_mul_f32 v[150:151], v[150:151], v[192:193]
	v_pk_mul_f32 v[148:149], v[148:149], v[190:191]
	v_pk_fma_f32 v[150:151], v[188:189], s[24:25], v[150:151] op_sel_hi:[1,0,1]
	v_pk_fma_f32 v[148:149], v[186:187], s[24:25], v[148:149] op_sel_hi:[1,0,1]
	v_mov_b32_e32 v189, v151
	v_pk_mov_b32 v[186:187], v[148:149], v[150:151] op_sel:[1,0]
	v_mov_b32_e32 v188, v148
	v_pk_add_f32 v[186:187], v[186:187], v[188:189]
	v_cvt_pk_f32_fp8_sdwa v[188:189], v35 src0_sel:WORD_1
	v_pk_add_f32 v[196:197], v[186:187], v[186:187] op_sel:[0,1] op_sel_hi:[1,0]
	v_cvt_pk_f32_fp8_e32 v[186:187], v35
	v_cvt_pk_f32_fp8_e32 v[190:191], v43
	v_cvt_pk_f32_fp8_sdwa v[192:193], v43 src0_sel:WORD_1
	v_cvt_pk_f32_fp8_e32 v[198:199], v27
	v_cvt_pk_f32_fp8_sdwa v[216:217], v27 src0_sel:WORD_1
	v_cvt_pk_f32_fp8_e32 v[218:219], v51
	v_cvt_pk_f32_fp8_sdwa v[220:221], v51 src0_sel:WORD_1
	v_cvt_pk_f32_fp8_e32 v[222:223], v19
	v_cvt_pk_f32_fp8_sdwa v[224:225], v19 src0_sel:WORD_1
	v_pk_fma_f32 v[188:189], s[44:45], v[188:189], 0 op_sel_hi:[0,1,0]
	v_pk_fma_f32 v[186:187], s[44:45], v[186:187], 0 op_sel_hi:[0,1,0]
	v_cvt_pk_f32_fp8_e32 v[226:227], v23
	v_cvt_pk_f32_fp8_sdwa v[228:229], v23 src0_sel:WORD_1
	v_pk_fma_f32 v[186:187], s[42:43], v[190:191], v[186:187] op_sel_hi:[0,1,1]
	v_pk_fma_f32 v[188:189], s[42:43], v[192:193], v[188:189] op_sel_hi:[0,1,1]
	v_cvt_pk_f32_fp8_e32 v[230:231], v31
	v_cvt_pk_f32_fp8_sdwa v[232:233], v31 src0_sel:WORD_1
	v_pk_fma_f32 v[188:189], s[40:41], v[216:217], v[188:189] op_sel_hi:[0,1,1]
	v_pk_fma_f32 v[186:187], s[40:41], v[198:199], v[186:187] op_sel_hi:[0,1,1]
	v_pk_fma_f32 v[186:187], s[38:39], v[218:219], v[186:187] op_sel_hi:[0,1,1]
	v_pk_fma_f32 v[188:189], s[38:39], v[220:221], v[188:189] op_sel_hi:[0,1,1]
	v_pk_fma_f32 v[188:189], s[36:37], v[224:225], v[188:189] op_sel_hi:[0,1,1]
	v_pk_fma_f32 v[186:187], s[36:37], v[222:223], v[186:187] op_sel_hi:[0,1,1]
	v_pk_fma_f32 v[186:187], s[2:3], v[226:227], v[186:187] op_sel_hi:[0,1,1]
	v_pk_fma_f32 v[188:189], s[2:3], v[228:229], v[188:189] op_sel_hi:[0,1,1]
	v_pk_add_f32 v[188:189], v[188:189], v[232:233]
	v_pk_add_f32 v[186:187], v[186:187], v[230:231]
	v_lshl_add_u64 v[198:199], v[180:181], 0, s[26:27]
	v_pk_mul_f32 v[190:191], v[186:187], s[22:23] op_sel_hi:[1,0]
	v_pk_mul_f32 v[192:193], v[188:189], s[22:23] op_sel_hi:[1,0]
	v_add_u32_e32 v247, s100, v198
	ds_read_b128 v[186:189], v247 offset:16
	s_waitcnt lgkmcnt(0)
; #define GAS __attribute__((address_space(1)))
; template <int l>
; __device__ __forceinline__ void layer_phases(Frame& F, const XcdBarrier& bar, const int lo, const int hi) {
;     ...
;                 for (int jh = 0; jh < 2; ++jh) {
; #pragma unroll
;                     for (int i = 0; i < 4; ++i) { const int j = 4 * jh + i, k = 16 * ln + 1024 * jh + 4 * i; f32x4 f = (f32x4){0.f, 0.f, 0.f, 0.f};
; #pragma unroll
;                         for (int q = 0; q < 7; ++q) { const unsigned w = yr[7 * jh + q][i]; const float gq = gt[q];
;                             const auto lo2 = __builtin_amdgcn_cvt_pk_f32_fp8((int)w, false), hi2 = __builtin_amdgcn_cvt_pk_f32_fp8((int)w, true);
;                             f.x += gq * lo2[0]; f.y += gq * lo2[1]; f.z += gq * hi2[0]; f.w += gq * hi2[1]; }
;                         v[j] = v[j] * ALPHA + *(const GAS f32x4*)(mrow + 10240 + k) * (f * (1.0f / (float)(1 << YSHIFT)));
;                         s += (v[j].x + v[j].y) + (v[j].z + v[j].w); }
	v_pk_mul_f32 v[144:145], v[144:145], v[190:191]
	v_cvt_pk_f32_fp8_e32 v[180:181], v36
	v_pk_fma_f32 v[144:145], v[182:183], s[24:25], v[144:145] op_sel_hi:[1,0,1]
	v_cvt_pk_f32_fp8_sdwa v[182:183], v36 src0_sel:WORD_1
	v_pk_mul_f32 v[146:147], v[146:147], v[192:193]
	v_cvt_pk_f32_fp8_e32 v[190:191], v44
	v_cvt_pk_f32_fp8_sdwa v[192:193], v44 src0_sel:WORD_1
	v_cvt_pk_f32_fp8_e32 v[218:219], v52
	v_cvt_pk_f32_fp8_sdwa v[220:221], v52 src0_sel:WORD_1
	v_cvt_pk_f32_fp8_e32 v[222:223], v56
	v_cvt_pk_f32_fp8_sdwa v[224:225], v56 src0_sel:WORD_1
	v_cvt_pk_f32_fp8_e32 v[226:227], v60
	v_cvt_pk_f32_fp8_sdwa v[228:229], v60 src0_sel:WORD_1
	v_pk_fma_f32 v[182:183], s[44:45], v[182:183], 0 op_sel_hi:[0,1,0]
	v_pk_fma_f32 v[180:181], s[44:45], v[180:181], 0 op_sel_hi:[0,1,0]
	v_cvt_pk_f32_fp8_e32 v[230:231], v64
	v_cvt_pk_f32_fp8_sdwa v[232:233], v64 src0_sel:WORD_1
	v_pk_fma_f32 v[180:181], s[42:43], v[190:191], v[180:181] op_sel_hi:[0,1,1]
	v_pk_fma_f32 v[182:183], s[42:43], v[192:193], v[182:183] op_sel_hi:[0,1,1]
	v_cvt_pk_f32_fp8_e32 v[234:235], v76
	v_cvt_pk_f32_fp8_sdwa v[236:237], v76 src0_sel:WORD_1
	v_pk_fma_f32 v[182:183], s[40:41], v[220:221], v[182:183] op_sel_hi:[0,1,1]
	v_pk_fma_f32 v[180:181], s[40:41], v[218:219], v[180:181] op_sel_hi:[0,1,1]
	v_pk_fma_f32 v[180:181], s[38:39], v[222:223], v[180:181] op_sel_hi:[0,1,1]
	v_pk_fma_f32 v[182:183], s[38:39], v[224:225], v[182:183] op_sel_hi:[0,1,1]
	v_pk_fma_f32 v[182:183], s[36:37], v[228:229], v[182:183] op_sel_hi:[0,1,1]
	v_pk_fma_f32 v[180:181], s[36:37], v[226:227], v[180:181] op_sel_hi:[0,1,1]
	v_pk_fma_f32 v[180:181], s[2:3], v[230:231], v[180:181] op_sel_hi:[0,1,1]
	v_pk_fma_f32 v[182:183], s[2:3], v[232:233], v[182:183] op_sel_hi:[0,1,1]
	v_pk_add_f32 v[218:219], v[182:183], v[236:237]
	v_pk_add_f32 v[220:221], v[180:181], v[234:235]
	v_add_u32_e32 v247, s100, v198
	ds_read_b128 v[180:183], v247 offset:48
	v_add_u32_e32 v247, s100, v198
	ds_read_b128 v[190:193], v247 offset:32
	v_pk_mul_f32 v[198:199], v[220:221], s[22:23] op_sel_hi:[1,0]
	v_pk_mul_f32 v[218:219], v[218:219], s[22:23] op_sel_hi:[1,0]
	s_waitcnt lgkmcnt(0)
	v_pk_mul_f32 v[198:199], v[212:213], v[198:199]
	v_pk_mul_f32 v[214:215], v[214:215], v[218:219]
	v_pk_fma_f32 v[146:147], v[184:185], s[24:25], v[146:147] op_sel_hi:[1,0,1]
	v_pk_fma_f32 v[168:169], v[168:169], s[24:25], v[214:215] op_sel_hi:[1,0,1]
	v_pk_fma_f32 v[170:171], v[170:171], s[24:25], v[198:199] op_sel_hi:[1,0,1]
	v_add_f32_e32 v184, v144, v145
	v_add_f32_e32 v216, v146, v147
	v_mov_b32_e32 v195, v170
	v_mov_b32_e32 v197, v171
	v_mov_b32_e32 v185, v168
	v_mov_b32_e32 v217, v169
	v_pk_add_f32 v[194:195], v[194:195], v[196:197]
	v_pk_add_f32 v[184:185], v[184:185], v[216:217]
	v_cvt_pk_f32_fp8_e32 v[198:199], v45
	v_pk_add_f32 v[184:185], v[194:195], v[184:185]
	v_cvt_pk_f32_fp8_e32 v[194:195], v37
	v_cvt_pk_f32_fp8_e32 v[214:215], v53
	v_cvt_pk_f32_fp8_e32 v[218:219], v57
	v_cvt_pk_f32_fp8_e32 v[222:223], v61
	v_pk_fma_f32 v[194:195], s[44:45], v[194:195], 0 op_sel_hi:[0,1,0]
	v_cvt_pk_f32_fp8_e32 v[226:227], v65
	v_pk_fma_f32 v[194:195], s[42:43], v[198:199], v[194:195] op_sel_hi:[0,1,1]
	v_cvt_pk_f32_fp8_sdwa v[196:197], v37 src0_sel:WORD_1
	v_cvt_pk_f32_fp8_e32 v[230:231], v77
	v_pk_fma_f32 v[194:195], s[40:41], v[214:215], v[194:195] op_sel_hi:[0,1,1]
	v_cvt_pk_f32_fp8_sdwa v[212:213], v45 src0_sel:WORD_1
	v_pk_fma_f32 v[194:195], s[38:39], v[218:219], v[194:195] op_sel_hi:[0,1,1]
	v_cvt_pk_f32_fp8_sdwa v[216:217], v53 src0_sel:WORD_1
	v_pk_fma_f32 v[194:195], s[36:37], v[222:223], v[194:195] op_sel_hi:[0,1,1]
	v_cvt_pk_f32_fp8_sdwa v[220:221], v57 src0_sel:WORD_1
	v_pk_fma_f32 v[194:195], s[2:3], v[226:227], v[194:195] op_sel_hi:[0,1,1]
	v_cvt_pk_f32_fp8_sdwa v[224:225], v61 src0_sel:WORD_1
	v_pk_fma_f32 v[196:197], s[44:45], v[196:197], 0 op_sel_hi:[0,1,0]
	v_pk_add_f32 v[194:195], v[194:195], v[230:231]
	v_cvt_pk_f32_fp8_sdwa v[228:229], v65 src0_sel:WORD_1
	v_pk_fma_f32 v[196:197], s[42:43], v[212:213], v[196:197] op_sel_hi:[0,1,1]
	v_pk_mul_f32 v[194:195], v[194:195], s[22:23] op_sel_hi:[1,0]
	v_cvt_pk_f32_fp8_sdwa v[232:233], v77 src0_sel:WORD_1
	v_pk_fma_f32 v[196:197], s[40:41], v[216:217], v[196:197] op_sel_hi:[0,1,1]
	v_pk_fma_f32 v[196:197], s[38:39], v[220:221], v[196:197] op_sel_hi:[0,1,1]
	v_cvt_pk_f32_fp8_sdwa v[198:199], v46 src0_sel:WORD_1
	v_pk_fma_f32 v[196:197], s[36:37], v[224:225], v[196:197] op_sel_hi:[0,1,1]
	v_cvt_pk_f32_fp8_sdwa v[214:215], v54 src0_sel:WORD_1
	v_pk_fma_f32 v[196:197], s[2:3], v[228:229], v[196:197] op_sel_hi:[0,1,1]
	v_cvt_pk_f32_fp8_sdwa v[218:219], v58 src0_sel:WORD_1
	s_waitcnt lgkmcnt(0)
	v_pk_mul_f32 v[186:187], v[186:187], v[194:195]
	v_cvt_pk_f32_fp8_sdwa v[194:195], v38 src0_sel:WORD_1
	v_pk_add_f32 v[196:197], v[196:197], v[232:233]
	v_cvt_pk_f32_fp8_sdwa v[222:223], v62 src0_sel:WORD_1
	v_pk_mul_f32 v[196:197], v[196:197], s[22:23] op_sel_hi:[1,0]
	v_pk_fma_f32 v[194:195], s[44:45], v[194:195], 0 op_sel_hi:[0,1,0]
	v_cvt_pk_f32_fp8_sdwa v[226:227], v66 src0_sel:WORD_1
	v_pk_fma_f32 v[194:195], s[42:43], v[198:199], v[194:195] op_sel_hi:[0,1,1]
	v_pk_mul_f32 v[188:189], v[188:189], v[196:197]
	v_cvt_pk_f32_fp8_sdwa v[230:231], v78 src0_sel:WORD_1
	v_pk_fma_f32 v[194:195], s[40:41], v[214:215], v[194:195] op_sel_hi:[0,1,1]
	v_pk_fma_f32 v[174:175], v[174:175], s[24:25], v[188:189] op_sel_hi:[1,0,1]
	v_pk_fma_f32 v[176:177], v[176:177], s[24:25], v[186:187] op_sel_hi:[1,0,1]
	v_pk_fma_f32 v[194:195], s[38:39], v[218:219], v[194:195] op_sel_hi:[0,1,1]
	v_pk_mov_b32 v[186:187], v[176:177], v[174:175] op_sel:[1,0]
	v_mov_b32_e32 v188, v176
	v_mov_b32_e32 v189, v175
	v_pk_fma_f32 v[194:195], s[36:37], v[222:223], v[194:195] op_sel_hi:[0,1,1]
	v_pk_add_f32 v[186:187], v[186:187], v[188:189]
	v_cvt_pk_f32_fp8_e32 v[188:189], v38
	v_pk_fma_f32 v[194:195], s[2:3], v[226:227], v[194:195] op_sel_hi:[0,1,1]
	v_cvt_pk_f32_fp8_e32 v[196:197], v46
	v_pk_add_f32 v[194:195], v[194:195], v[230:231]
	v_cvt_pk_f32_fp8_e32 v[212:213], v54
	v_pk_mul_f32 v[194:195], v[194:195], s[22:23] op_sel_hi:[1,0]
	v_cvt_pk_f32_fp8_e32 v[216:217], v58
	v_cvt_pk_f32_fp8_e32 v[220:221], v62
	v_pk_fma_f32 v[188:189], s[44:45], v[188:189], 0 op_sel_hi:[0,1,0]
	v_cvt_pk_f32_fp8_e32 v[224:225], v66
	v_pk_fma_f32 v[188:189], s[42:43], v[196:197], v[188:189] op_sel_hi:[0,1,1]
	v_cvt_pk_f32_fp8_e32 v[196:197], v47
	v_cvt_pk_f32_fp8_sdwa v[198:199], v47 src0_sel:WORD_1
	s_waitcnt lgkmcnt(0)
; #define GAS __attribute__((address_space(1)))
; template <int l>
; __device__ __forceinline__ void layer_phases(Frame& F, const XcdBarrier& bar, const int lo, const int hi) {
;     ...
;                 for (int jh = 0; jh < 2; ++jh) {
; #pragma unroll
;                     for (int i = 0; i < 4; ++i) { const int j = 4 * jh + i, k = 16 * ln + 1024 * jh + 4 * i; f32x4 f = (f32x4){0.f, 0.f, 0.f, 0.f};
; #pragma unroll
;                         for (int q = 0; q < 7; ++q) { const unsigned w = yr[7 * jh + q][i]; const float gq = gt[q];
;                             const auto lo2 = __builtin_amdgcn_cvt_pk_f32_fp8((int)w, false), hi2 = __builtin_amdgcn_cvt_pk_f32_fp8((int)w, true);
;                             f.x += gq * lo2[0]; f.y += gq * lo2[1]; f.z += gq * hi2[0]; f.w += gq * hi2[1]; }
;                         v[j] = v[j] * ALPHA + *(const GAS f32x4*)(mrow + 10240 + k) * (f * (1.0f / (float)(1 << YSHIFT)));
;                         s += (v[j].x + v[j].y) + (v[j].z + v[j].w); }
;                 }
;                 const float mean = wave_sum(s) * (1.f / D); float s2 = 0.f;
; #pragma unroll
;                 for (int j = 0; j < 8; ++j) { v[j] = v[j] - mean; s2 += (v[j].x * v[j].x + v[j].y * v[j].y) + (v[j].z * v[j].z + v[j].w * v[j].w); }
	v_pk_mul_f32 v[192:193], v[192:193], v[194:195]
	v_cvt_pk_f32_fp8_sdwa v[194:195], v39 src0_sel:WORD_1
	v_pk_fma_f32 v[178:179], v[178:179], s[24:25], v[192:193] op_sel_hi:[1,0,1]
	v_cvt_pk_f32_fp8_e32 v[192:193], v39
	v_cvt_pk_f32_fp8_e32 v[228:229], v78
	v_pk_fma_f32 v[188:189], s[40:41], v[212:213], v[188:189] op_sel_hi:[0,1,1]
	v_cvt_pk_f32_fp8_e32 v[212:213], v55
	v_cvt_pk_f32_fp8_sdwa v[214:215], v55 src0_sel:WORD_1
	v_pk_fma_f32 v[188:189], s[38:39], v[216:217], v[188:189] op_sel_hi:[0,1,1]
	v_cvt_pk_f32_fp8_e32 v[216:217], v59
	v_cvt_pk_f32_fp8_sdwa v[218:219], v59 src0_sel:WORD_1
	v_pk_fma_f32 v[188:189], s[36:37], v[220:221], v[188:189] op_sel_hi:[0,1,1]
	v_cvt_pk_f32_fp8_e32 v[220:221], v63
	v_cvt_pk_f32_fp8_sdwa v[222:223], v63 src0_sel:WORD_1
	v_pk_fma_f32 v[194:195], s[44:45], v[194:195], 0 op_sel_hi:[0,1,0]
	v_pk_fma_f32 v[192:193], s[44:45], v[192:193], 0 op_sel_hi:[0,1,0]
	v_pk_fma_f32 v[188:189], s[2:3], v[224:225], v[188:189] op_sel_hi:[0,1,1]
	v_cvt_pk_f32_fp8_e32 v[224:225], v67
	v_cvt_pk_f32_fp8_sdwa v[226:227], v67 src0_sel:WORD_1
	v_pk_fma_f32 v[192:193], s[42:43], v[196:197], v[192:193] op_sel_hi:[0,1,1]
	v_pk_fma_f32 v[194:195], s[42:43], v[198:199], v[194:195] op_sel_hi:[0,1,1]
	v_pk_add_f32 v[188:189], v[188:189], v[228:229]
	v_cvt_pk_f32_fp8_e32 v[228:229], v79
	v_cvt_pk_f32_fp8_sdwa v[230:231], v79 src0_sel:WORD_1
	v_pk_fma_f32 v[194:195], s[40:41], v[214:215], v[194:195] op_sel_hi:[0,1,1]
	v_pk_fma_f32 v[192:193], s[40:41], v[212:213], v[192:193] op_sel_hi:[0,1,1]
	v_pk_fma_f32 v[192:193], s[38:39], v[216:217], v[192:193] op_sel_hi:[0,1,1]
	v_pk_fma_f32 v[194:195], s[38:39], v[218:219], v[194:195] op_sel_hi:[0,1,1]
	v_pk_fma_f32 v[194:195], s[36:37], v[222:223], v[194:195] op_sel_hi:[0,1,1]
	v_pk_fma_f32 v[192:193], s[36:37], v[220:221], v[192:193] op_sel_hi:[0,1,1]
	v_pk_fma_f32 v[192:193], s[2:3], v[224:225], v[192:193] op_sel_hi:[0,1,1]
	v_pk_fma_f32 v[194:195], s[2:3], v[226:227], v[194:195] op_sel_hi:[0,1,1]
	v_pk_add_f32 v[194:195], v[194:195], v[230:231]
	v_pk_add_f32 v[192:193], v[192:193], v[228:229]
	v_pk_mul_f32 v[188:189], v[188:189], s[22:23] op_sel_hi:[1,0]
	v_pk_mul_f32 v[192:193], v[192:193], s[22:23] op_sel_hi:[1,0]
	v_pk_mul_f32 v[194:195], v[194:195], s[22:23] op_sel_hi:[1,0]
	v_and_b32_e32 v167, 0xffff0000, v11
	v_pk_mul_f32 v[188:189], v[190:191], v[188:189]
	v_pk_mul_f32 v[182:183], v[182:183], v[194:195]
	v_pk_mul_f32 v[180:181], v[180:181], v[192:193]
	v_pk_add_f32 v[184:185], v[184:185], v[184:185] op_sel:[0,1] op_sel_hi:[1,0]
	v_pk_add_f32 v[186:187], v[186:187], v[186:187] op_sel:[0,1] op_sel_hi:[1,0]
	v_pk_fma_f32 v[172:173], v[172:173], s[24:25], v[188:189] op_sel_hi:[1,0,1]
	v_pk_fma_f32 v[166:167], v[166:167], s[24:25], v[182:183] op_sel_hi:[1,0,1]
	v_pk_fma_f32 v[164:165], v[164:165], s[24:25], v[180:181] op_sel_hi:[1,0,1]
	v_add_f32_e32 v188, v172, v173
	v_add_f32_e32 v190, v178, v179
	v_mov_b32_e32 v185, v164
	v_mov_b32_e32 v187, v165
	v_mov_b32_e32 v189, v166
	v_mov_b32_e32 v191, v167
	v_pk_add_f32 v[180:181], v[184:185], v[186:187]
	v_pk_add_f32 v[182:183], v[188:189], v[190:191]
	v_lshl_add_u64 v[188:189], s[8:9], 0, v[162:163]
	v_pk_add_f32 v[180:181], v[180:181], v[182:183]
	v_lshl_add_u64 v[190:191], s[10:11], 0, v[162:163]
	v_add_f32_e32 v161, v180, v181
	ds_bpermute_b32 v180, v203, v161
	s_ashr_i32 s35, s34, 31
	s_waitcnt lgkmcnt(0)
	v_add_f32_e32 v161, v161, v180
	ds_bpermute_b32 v180, v204, v161
	s_waitcnt lgkmcnt(0)
	v_add_f32_e32 v161, v161, v180
	ds_bpermute_b32 v180, v205, v161
	s_waitcnt lgkmcnt(0)
	v_add_f32_e32 v161, v161, v180
	ds_bpermute_b32 v180, v206, v161
	s_waitcnt lgkmcnt(0)
	v_add_f32_e32 v161, v161, v180
	ds_bpermute_b32 v180, v207, v161
	s_waitcnt lgkmcnt(0)
	v_add_f32_e32 v161, v161, v180
	ds_bpermute_b32 v180, v208, v161
	s_waitcnt lgkmcnt(0)
	v_add_f32_e32 v161, v161, v180
	v_fmamk_f32 v159, v161, 0xba000000, v159
	v_fmamk_f32 v155, v161, 0xba000000, v155
	v_fmamk_f32 v157, v161, 0xba000000, v157
	v_fmac_f32_e32 v158, 0xba000000, v161
	v_fmamk_f32 v153, v161, 0xba000000, v153
	v_fmac_f32_e32 v154, 0xba000000, v161
	v_mov_b32_e32 v182, v159
	v_mov_b32_e32 v183, v155
	v_fmac_f32_e32 v156, 0xba000000, v161
	v_fmac_f32_e32 v152, 0xba000000, v161
	v_mov_b32_e32 v180, v158
	v_mov_b32_e32 v181, v154
	v_pk_mul_f32 v[182:183], v[182:183], v[182:183]
	v_mov_b32_e32 v184, v157
	v_mov_b32_e32 v185, v153
	v_pk_fma_f32 v[180:181], v[180:181], v[180:181], v[182:183]
	v_mov_b32_e32 v182, v156
	v_mov_b32_e32 v183, v152
	v_pk_mul_f32 v[184:185], v[184:185], v[184:185]
	v_fmamk_f32 v149, v161, 0xba000000, v149
	v_pk_fma_f32 v[182:183], v[182:183], v[182:183], v[184:185]
	v_fmac_f32_e32 v148, 0xba000000, v161
	v_pk_add_f32 v[180:181], v[180:181], v[182:183]
	v_fmamk_f32 v151, v161, 0xba000000, v151
	v_fmac_f32_e32 v150, 0xba000000, v161
	v_pk_add_f32 v[180:181], v[180:181], v[180:181] op_sel_hi:[0,1]
	v_pk_mul_f32 v[182:183], v[150:151], v[150:151]
	v_pk_mul_f32 v[184:185], v[148:149], v[148:149]
	v_fmac_f32_e32 v144, 0xba000000, v161
	v_pk_mov_b32 v[186:187], v[184:185], v[182:183] op_sel:[1,0]
	v_mov_b32_e32 v185, v183
	v_fmamk_f32 v145, v161, 0xba000000, v145
	v_fmac_f32_e32 v146, 0xba000000, v161
	v_mul_f32_e32 v180, v144, v144
	v_pk_add_f32 v[182:183], v[186:187], v[184:185]
	v_fmamk_f32 v147, v161, 0xba000000, v147
	v_pk_fma_f32 v[184:185], v[144:145], v[144:145], v[180:181] op_sel_hi:[1,1,0]
	v_mul_f32_e32 v180, v146, v146
	v_pk_add_f32 v[182:183], v[182:183], v[182:183] op_sel_hi:[0,1]
	v_pk_fma_f32 v[186:187], v[146:147], v[146:147], v[180:181] op_sel_hi:[1,1,0]
	v_fmamk_f32 v169, v161, 0xba000000, v169
	v_fmac_f32_e32 v168, 0xba000000, v161
; #define GAS __attribute__((address_space(1)))
; template <int l>
; __device__ __forceinline__ void layer_phases(Frame& F, const XcdBarrier& bar, const int lo, const int hi) {
;     ...
;                 const float mean = wave_sum(s) * (1.f / D); float s2 = 0.f;
; #pragma unroll
;                 for (int j = 0; j < 8; ++j) { v[j] = v[j] - mean; s2 += (v[j].x * v[j].x + v[j].y * v[j].y) + (v[j].z * v[j].z + v[j].w * v[j].w); }
;                 const float rstd = 1.f / sqrtf(wave_sum(s2) * (1.f / D) + LN_EPS);
;                 float* orow = Fout + (size_t)m * D;
; #pragma unroll
;                 for (int j = 0; j < 8; ++j) { const int k = 16 * ln + 1024 * (j >> 2) + 4 * (j & 3);
;                     v[j] = v[j] * rstd * *(const GAS f32x4*)(g2 + k) + *(const GAS f32x4*)(b2 + k);
;                     if (l == 1) { *(GAS f32x4*)(orow + k) = v[j]; if (j & 1) asm volatile("" ::: "memory"); } }
;     ...
;                 for (int m_ = gw; m_ < T; m_ += 2 * NGW) {
;                     const bool hasB = m_ + NGW < T;
;                     if (hasB) load_row(row_of(m_ + NGW), xB, yB, gB);
;                     process_row(row_of(m_), xA, yA, gA);
;                     if (m_ + 2 * NGW < T) load_row(row_of(m_ + 2 * NGW), xA, yA, gA);
	v_fmamk_f32 v171, v161, 0xba000000, v171
	v_fmac_f32_e32 v170, 0xba000000, v161
	v_mul_f32_e32 v184, v170, v170
	v_mul_f32_e32 v186, v171, v171
	v_mul_f32_e32 v182, v168, v168
	v_mul_f32_e32 v180, v169, v169
	v_pk_add_f32 v[184:185], v[184:185], v[186:187]
	v_pk_add_f32 v[180:181], v[182:183], v[180:181]
	v_fmamk_f32 v177, v161, 0xba000000, v177
	v_pk_add_f32 v[180:181], v[184:185], v[180:181]
	v_fmac_f32_e32 v176, 0xba000000, v161
	v_fmamk_f32 v175, v161, 0xba000000, v175
	v_fmac_f32_e32 v174, 0xba000000, v161
	v_pk_add_f32 v[180:181], v[180:181], v[180:181] op_sel_hi:[0,1]
	v_pk_mul_f32 v[182:183], v[174:175], v[174:175]
	v_pk_mul_f32 v[184:185], v[176:177], v[176:177]
	v_fmac_f32_e32 v172, 0xba000000, v161
	v_pk_mov_b32 v[186:187], v[184:185], v[182:183] op_sel:[1,0]
	v_mov_b32_e32 v185, v183
	v_fmamk_f32 v173, v161, 0xba000000, v173
	v_fmac_f32_e32 v178, 0xba000000, v161
	v_mul_f32_e32 v180, v172, v172
	v_pk_add_f32 v[182:183], v[186:187], v[184:185]
	v_fmamk_f32 v179, v161, 0xba000000, v179
	v_pk_fma_f32 v[184:185], v[172:173], v[172:173], v[180:181] op_sel_hi:[1,1,0]
	v_mul_f32_e32 v180, v178, v178
	v_pk_add_f32 v[182:183], v[182:183], v[182:183] op_sel_hi:[0,1]
	v_pk_fma_f32 v[186:187], v[178:179], v[178:179], v[180:181] op_sel_hi:[1,1,0]
	v_fmamk_f32 v167, v161, 0xba000000, v167
	v_fmac_f32_e32 v166, 0xba000000, v161
	v_fmamk_f32 v165, v161, 0xba000000, v165
	v_fmac_f32_e32 v164, 0xba000000, v161
	v_mul_f32_e32 v184, v164, v164
	v_mul_f32_e32 v186, v165, v165
	v_mul_f32_e32 v182, v166, v166
	v_mul_f32_e32 v180, v167, v167
	v_pk_add_f32 v[184:185], v[184:185], v[186:187]
	v_pk_add_f32 v[180:181], v[182:183], v[180:181]
	s_nop 0
	v_pk_add_f32 v[180:181], v[184:185], v[180:181]
	v_add_u32_e32 v247, s99, v190
	ds_read_b128 v[184:187], v247
	v_add_f32_e32 v161, v180, v181
	v_add_u32_e32 v247, s98, v188
	ds_read_b128 v[180:183], v247
	ds_bpermute_b32 v192, v203, v161
	s_waitcnt lgkmcnt(0)
	v_add_f32_e32 v161, v161, v192
	ds_bpermute_b32 v192, v204, v161
	s_waitcnt lgkmcnt(0)
	v_add_f32_e32 v161, v161, v192
	ds_bpermute_b32 v192, v205, v161
	s_waitcnt lgkmcnt(0)
	v_add_f32_e32 v161, v161, v192
	ds_bpermute_b32 v192, v206, v161
	s_waitcnt lgkmcnt(0)
	v_add_f32_e32 v161, v161, v192
	ds_bpermute_b32 v192, v207, v161
	s_waitcnt lgkmcnt(0)
	v_add_f32_e32 v161, v161, v192
	ds_bpermute_b32 v192, v208, v161
	s_waitcnt lgkmcnt(0)
	v_add_f32_e32 v161, v161, v192
	v_fmamk_f32 v161, v161, 0x3a000000, v209
	v_mul_f32_e32 v192, 0x4f800000, v161
	v_cmp_gt_f32_e32 vcc, s55, v161
	s_nop 1
	v_cndmask_b32_e32 v161, v161, v192, vcc
	v_sqrt_f32_e32 v192, v161
	s_nop 0
	v_add_u32_e32 v193, -1, v192
	v_fma_f32 v194, -v193, v192, v161
	v_cmp_ge_f32_e64 s[2:3], 0, v194
	v_add_u32_e32 v194, 1, v192
	s_nop 0
	v_cndmask_b32_e64 v193, v192, v193, s[2:3]
	v_fma_f32 v192, -v194, v192, v161
	v_cmp_lt_f32_e64 s[2:3], 0, v192
	s_nop 1
	v_cndmask_b32_e64 v192, v193, v194, s[2:3]
	v_mul_f32_e32 v193, 0x37800000, v192
	v_cndmask_b32_e32 v192, v192, v193, vcc
	v_cmp_class_f32_e32 vcc, v161, v210
	s_nop 1
	v_cndmask_b32_e32 v161, v192, v161, vcc
	v_div_scale_f32 v192, s[2:3], v161, v161, 1.0
	v_rcp_f32_e32 v193, v192
	s_lshl_b64 s[2:3], s[34:35], 13
	s_add_u32 s2, s25, s2
	s_addc_u32 s3, s23, s3
	v_fma_f32 v194, -v192, v193, 1.0
	v_fmac_f32_e32 v193, v194, v193
	v_div_scale_f32 v194, vcc, 1.0, v161, 1.0
	v_mul_f32_e32 v195, v194, v193
	v_fma_f32 v196, -v192, v195, v194
	v_fmac_f32_e32 v195, v196, v193
	v_fma_f32 v192, -v192, v195, v194
	v_div_fmas_f32 v192, v192, v193, v195
	v_div_fixup_f32 v192, v192, v161, 1.0
	v_pk_mul_f32 v[194:195], v[158:159], v[192:193] op_sel_hi:[1,0]
	v_pk_mul_f32 v[156:157], v[156:157], v[192:193] op_sel_hi:[1,0]
	v_lshl_add_u64 v[162:163], s[2:3], 0, v[162:163]
	s_waitcnt lgkmcnt(0)
	v_pk_fma_f32 v[158:159], v[182:183], v[156:157], v[186:187]
	v_pk_fma_f32 v[156:157], v[180:181], v[194:195], v[184:185]
	global_store_dwordx4 v[162:163], v[156:159], off
	v_pk_mul_f32 v[184:185], v[152:153], v[192:193] op_sel_hi:[1,0]
	v_pk_mul_f32 v[152:153], v[154:155], v[192:193] op_sel_hi:[1,0]
	v_or_b32_e32 v156, 4, v160
	v_ashrrev_i32_e32 v157, 31, v156
	v_lshlrev_b64 v[180:181], 2, v[156:157]
	v_lshl_add_u64 v[156:157], s[8:9], 0, v[180:181]
	v_lshl_add_u64 v[180:181], s[10:11], 0, v[180:181]
	v_add_u32_e32 v247, s98, v156
	ds_read_b128 v[156:159], v247
	v_pk_mul_f32 v[150:151], v[150:151], v[192:193] op_sel_hi:[1,0]
	v_add_u32_e32 v247, s99, v180
	ds_read_b128 v[180:183], v247
	v_pk_mul_f32 v[148:149], v[148:149], v[192:193] op_sel_hi:[1,0]
	v_pk_mul_f32 v[146:147], v[146:147], v[192:193] op_sel_hi:[1,0]
	v_pk_mul_f32 v[144:145], v[144:145], v[192:193] op_sel_hi:[1,0]
	s_add_i32 s42, s79, s50
	s_cmpk_gt_i32 s42, 0x3fff
	s_waitcnt lgkmcnt(0)
; #define GAS __attribute__((address_space(1)))
; template <int l>
; __device__ __forceinline__ void layer_phases(Frame& F, const XcdBarrier& bar, const int lo, const int hi) {
;     ...
; #pragma unroll
;                 for (int j = 0; j < 8; ++j) { const int k = 16 * ln + 1024 * (j >> 2) + 4 * (j & 3);
;                     v[j] = v[j] * rstd * *(const GAS f32x4*)(g2 + k) + *(const GAS f32x4*)(b2 + k);
;                     if (l == 1) { *(GAS f32x4*)(orow + k) = v[j]; if (j & 1) asm volatile("" ::: "memory"); } }
;     ...
;                     if (m_ + 2 * NGW < T) load_row(row_of(m_ + 2 * NGW), xA, yA, gA);
	v_pk_fma_f32 v[152:153], v[156:157], v[152:153], v[180:181]
	v_pk_fma_f32 v[154:155], v[158:159], v[184:185], v[182:183]
	global_store_dwordx4 v[162:163], v[152:155], off offset:16
	s_nop 1
	v_or_b32_e32 v152, 8, v160
	v_ashrrev_i32_e32 v153, 31, v152
	v_lshlrev_b64 v[156:157], 2, v[152:153]
	v_lshl_add_u64 v[152:153], s[8:9], 0, v[156:157]
	v_lshl_add_u64 v[156:157], s[10:11], 0, v[156:157]
	v_add_u32_e32 v247, s98, v152
	ds_read_b128 v[152:155], v247
	s_nop 0
	v_add_u32_e32 v247, s99, v156
	ds_read_b128 v[156:159], v247
	s_waitcnt lgkmcnt(0)
	v_pk_fma_f32 v[148:149], v[152:153], v[148:149], v[156:157]
	v_pk_fma_f32 v[150:151], v[154:155], v[150:151], v[158:159]
	global_store_dwordx4 v[162:163], v[148:151], off offset:32
	s_nop 1
	v_or_b32_e32 v148, 12, v160
	v_ashrrev_i32_e32 v149, 31, v148
	v_lshlrev_b64 v[152:153], 2, v[148:149]
	v_lshl_add_u64 v[148:149], s[8:9], 0, v[152:153]
	v_lshl_add_u64 v[152:153], s[10:11], 0, v[152:153]
	v_add_u32_e32 v247, s98, v148
	ds_read_b128 v[148:151], v247
	s_nop 0
	v_add_u32_e32 v247, s99, v152
	ds_read_b128 v[152:155], v247
	s_waitcnt lgkmcnt(0)
	v_pk_fma_f32 v[144:145], v[148:149], v[144:145], v[152:153]
	v_pk_fma_f32 v[146:147], v[150:151], v[146:147], v[154:155]
	global_store_dwordx4 v[162:163], v[144:147], off offset:48
	v_pk_mul_f32 v[154:155], v[170:171], v[192:193] op_sel_hi:[1,0]
	v_pk_mul_f32 v[152:153], v[168:169], v[192:193] op_sel_hi:[1,0]
	v_add_co_u32_e32 v144, vcc, s51, v188
	v_pk_mul_f32 v[168:169], v[176:177], v[192:193] op_sel_hi:[1,0]
	s_nop 0
	v_addc_co_u32_e32 v145, vcc, 0, v189, vcc
	v_add_co_u32_e32 v148, vcc, s51, v190
	v_add_u32_e32 v247, s98, v144
	ds_read_b128 v[144:147], v247
	s_nop 0
	v_addc_co_u32_e32 v149, vcc, 0, v191, vcc
	v_add_u32_e32 v247, s99, v148
	ds_read_b128 v[148:151], v247
	s_waitcnt lgkmcnt(0)
	v_pk_fma_f32 v[144:145], v[144:145], v[154:155], v[148:149]
	v_add_co_u32_e32 v148, vcc, s51, v162
	v_pk_fma_f32 v[146:147], v[146:147], v[152:153], v[150:151]
	s_nop 0
	v_addc_co_u32_e32 v149, vcc, 0, v163, vcc
	global_store_dwordx4 v[148:149], v[144:147], off
	v_add_u32_e32 v154, 0x408, v160
	v_pk_mul_f32 v[162:163], v[174:175], v[192:193] op_sel_hi:[1,0]
	v_add_u32_e32 v144, 0x404, v160
	v_ashrrev_i32_e32 v145, 31, v144
	v_lshlrev_b64 v[152:153], 2, v[144:145]
	v_lshl_add_u64 v[144:145], s[8:9], 0, v[152:153]
	v_lshl_add_u64 v[148:149], s[10:11], 0, v[152:153]
	v_add_u32_e32 v247, s98, v144
	ds_read_b128 v[144:147], v247
	v_ashrrev_i32_e32 v155, 31, v154
	v_add_u32_e32 v247, s99, v148
	ds_read_b128 v[148:151], v247
	v_lshl_add_u64 v[152:153], s[2:3], 0, v[152:153]
	v_lshlrev_b64 v[154:155], 2, v[154:155]
	v_lshl_add_u64 v[156:157], s[8:9], 0, v[154:155]
	v_lshl_add_u64 v[158:159], s[10:11], 0, v[154:155]
	v_lshl_add_u64 v[154:155], s[2:3], 0, v[154:155]
	s_waitcnt lgkmcnt(0)
	v_pk_fma_f32 v[144:145], v[144:145], v[168:169], v[148:149]
	v_pk_fma_f32 v[146:147], v[146:147], v[162:163], v[150:151]
	global_store_dwordx4 v[152:153], v[144:147], off
	v_add_u32_e32 v247, s98, v156
	ds_read_b128 v[144:147], v247
	v_add_u32_e32 v247, s99, v158
	ds_read_b128 v[148:151], v247
	v_add_u32_e32 v152, 0x40c, v160
	v_ashrrev_i32_e32 v153, 31, v152
	v_pk_mul_f32 v[160:161], v[178:179], v[192:193] op_sel_hi:[1,0]
	v_pk_mul_f32 v[162:163], v[172:173], v[192:193] op_sel_hi:[1,0]
	v_lshlrev_b64 v[152:153], 2, v[152:153]
	v_lshl_add_u64 v[156:157], s[8:9], 0, v[152:153]
	v_lshl_add_u64 v[158:159], s[10:11], 0, v[152:153]
	v_lshl_add_u64 v[152:153], s[2:3], 0, v[152:153]
	s_cselect_b64 s[2:3], -1, 0
	s_and_b64 vcc, exec, s[2:3]
	s_waitcnt lgkmcnt(0)
	v_pk_fma_f32 v[144:145], v[144:145], v[162:163], v[148:149]
	v_pk_fma_f32 v[146:147], v[146:147], v[160:161], v[150:151]
	global_store_dwordx4 v[154:155], v[144:147], off
	v_add_u32_e32 v247, s98, v156
	ds_read_b128 v[144:147], v247
	s_nop 0
	v_add_u32_e32 v247, s99, v158
	ds_read_b128 v[148:151], v247
	v_pk_mul_f32 v[154:155], v[166:167], v[192:193] op_sel_hi:[1,0]
	v_pk_mul_f32 v[156:157], v[164:165], v[192:193] op_sel_hi:[1,0]
	s_waitcnt lgkmcnt(0)
	v_pk_fma_f32 v[146:147], v[146:147], v[154:155], v[150:151]
	v_pk_fma_f32 v[144:145], v[144:145], v[156:157], v[148:149]
	global_store_dwordx4 v[152:153], v[144:147], off
	s_cbranch_vccnz .LBB0_1895
	s_and_b64 vcc, exec, s[0:1]
	s_mov_b32 s34, s42
	s_cbranch_vccnz .LBB0_1892
	s_lshr_b32 s33, s79, 3
	s_ashr_i32 s34, s42, 3
	s_and_b32 s29, s45, 0x3800
	s_and_b32 s33, s33, 0xf8
	s_and_b32 s34, s34, 0xffffff00
	s_or_b32 s33, s33, s34
	s_or_b32 s29, s29, s43
	s_add_i32 s34, s29, s33

; template <int l>
; __device__ __forceinline__ void layer_phases(Frame& F, const XcdBarrier& bar, const int lo, const int hi) {
;     ...
;                     if (hasB) load_row(row_of(m_ + NGW), xB, yB, gB);
;                     process_row(row_of(m_), xA, yA, gA);
;                     if (m_ + 2 * NGW < T) load_row(row_of(m_ + 2 * NGW), xA, yA, gA);
;                     if (hasB) process_row(row_of(m_ + NGW), xB, yB, gB);
;                 }
.LBB0_1894:
	s_or_b64 exec, exec, s[36:37]
	s_lshl_b64 s[36:37], s[34:35], 12
	s_add_u32 s36, s48, s36
	s_addc_u32 s37, s49, s37
	s_mul_i32 s33, s34, 0x3800
	v_lshlrev_b32_e32 v16, 4, v0
	s_mul_hi_i32 s29, s34, 0x3800
	s_add_u32 s34, s46, s33
	v_ashrrev_i32_e32 v17, 31, v16
	s_addc_u32 s35, s47, s29
	v_lshl_add_u64 v[44:45], s[34:35], 0, v[16:17]
	v_add_co_u32_e32 v48, vcc, s51, v44
	v_lshl_add_u64 v[12:13], v[16:17], 1, s[36:37]
	s_nop 0
	v_addc_co_u32_e32 v49, vcc, 0, v45, vcc
	v_add_co_u32_e32 v24, vcc, s52, v44
	v_lshl_add_u64 v[52:53], v[44:45], 0, s[12:13]
	s_nop 0
	v_addc_co_u32_e32 v25, vcc, 0, v45, vcc
	v_add_co_u32_e32 v28, vcc, 0x3000, v44
	v_lshl_add_u64 v[56:57], v[44:45], 0, s[14:15]
	v_lshl_add_u64 v[60:61], v[44:45], 0, s[6:7]
	v_lshl_add_u64 v[64:65], v[44:45], 0, s[16:17]
	v_lshl_add_u64 v[76:77], v[44:45], 0, s[18:19]
	v_addc_co_u32_e32 v29, vcc, 0, v45, vcc
	global_load_dwordx4 v[0:3], v[12:13], off offset:16 nt
	global_load_dwordx4 v[4:7], v[12:13], off nt
	global_load_dwordx4 v[8:11], v[12:13], off offset:2064 nt
	s_nop 0
	global_load_dwordx4 v[12:15], v[12:13], off offset:2048 nt
	s_nop 0
	global_load_dwordx4 v[16:19], v[24:25], off nt
	global_load_dwordx4 v[20:23], v[24:25], off offset:2048 nt
	s_nop 0
	global_load_dwordx4 v[24:27], v[24:25], off offset:-4096 nt
	s_nop 0
	global_load_dwordx4 v[28:31], v[28:29], off nt
	s_nop 0
	global_load_dwordx4 v[32:35], v[44:45], off nt
	global_load_dwordx4 v[36:39], v[44:45], off offset:1024 nt
	global_load_dwordx4 v[40:43], v[44:45], off offset:2048 nt
	s_nop 0
	global_load_dwordx4 v[44:47], v[44:45], off offset:3072 nt
	s_nop 0
	global_load_dwordx4 v[48:51], v[48:49], off offset:2048 nt
	s_nop 0
	global_load_dwordx4 v[52:55], v[52:53], off offset:1024 nt
	s_nop 0
	global_load_dwordx4 v[56:59], v[56:57], off offset:1024 nt
	s_nop 0
	global_load_dwordx4 v[60:63], v[60:61], off offset:1024 nt
	s_nop 0
	global_load_dwordx4 v[64:67], v[64:65], off offset:1024 nt
	s_nop 0
	global_load_dwordx4 v[76:79], v[76:77], off offset:1024 nt
	s_waitcnt vmcnt(27)
	s_andn2_b64 vcc, exec, s[30:31]
	s_cbranch_vccnz .LBB0_1880
	s_branch .LBB0_1896
.LBB0_1895:
	s_waitcnt vmcnt(8)
	s_andn2_b64 vcc, exec, s[30:31]
	s_cbranch_vccnz .LBB0_1880
.LBB0_1896:
	s_and_b64 vcc, exec, s[0:1]
	s_cbranch_vccnz .LBB0_1879
	s_lshr_b32 s1, s79, 3
	s_ashr_i32 s28, s28, 3
	s_and_b32 s0, s45, 0x3800
	s_and_b32 s1, s1, 0xf8
	s_and_b32 s28, s28, 0xffffff00
	s_or_b32 s1, s1, s28
	s_or_b32 s0, s0, s43
	s_add_i32 s28, s0, s1
	s_branch .LBB0_1879
.Lp8b_skipB:
	s_waitcnt vmcnt(0)
	s_branch .LBB0_1887
.LBB0_1898:
	s_barrier
